# wave-wide sum/max butterflies (P1, P7a, P8 tiles, P11a, P12): ds_bpermute round trips replaced by DPP quad_perm/row mirrors + v_permlane16/32_swap, same pairing tree (bitwise identical); on top of P6
# baseline (speedup 1.0000x reference)
; DI float wave_sum(float v) {
; #pragma unroll
;     for (int o = 1; o < 64; o <<= 1) v += __shfl_xor(v, o);
;     return v;
; __global__ void __launch_bounds__(NWAVES * 64, 2) fwd_kernel(Args a_unused) {
;     ...
;                 float ss = 0.f;
; #pragma unroll
;                 for (int j = 0; j < 8; ++j) ss += v[j][0] * v[j][0] + v[j][1] * v[j][1] + v[j][2] * v[j][2] + v[j][3] * v[j][3];
;                 const float rstd = rsqrtf(wave_sum(ss) * (1.0f / D) + EPS);
;                 float am = 0.f;
; #pragma unroll
;                 for (int j = 0; j < 8; ++j) { v[j] = v[j] * rstd * ca[j] + cb[j]; am = fmaxf(am, fmaxf(fmaxf(fabsf(v[j][0]), fabsf(v[j][1])), fmaxf(fabsf(v[j][2]), fabsf(v[j][3])))); }
; #pragma unroll
;                 for (int o = 1; o < 64; o <<= 1) am = fmaxf(am, __shfl_xor(am, o));
;                 if (am == 0.f) am = 1.f;
;                 const float qi = 127.0f / am;
;                 if (lane == 0) ((float*)(ws + WS_CS + CS_HROW))[m] = am * (1.0f / 127.0f);
.LBB0_233:
	s_waitcnt vmcnt(4)
	v_mul_f32_e32 v148, v95, v95
	v_mul_f32_e32 v149, v91, v91
	v_fmac_f32_e32 v148, v94, v94
	v_fmac_f32_e32 v149, v90, v90
	v_fmac_f32_e32 v148, v96, v96
	v_fmac_f32_e32 v149, v92, v92
	v_fmac_f32_e32 v148, v97, v97
	v_fmac_f32_e32 v149, v93, v93
	v_add_f32_e32 v148, v148, v149
	v_mul_f32_e32 v149, v87, v87
	v_fmac_f32_e32 v149, v86, v86
	v_fmac_f32_e32 v149, v88, v88
	v_fmac_f32_e32 v149, v89, v89
	v_add_f32_e32 v148, v148, v149
	v_mul_f32_e32 v149, v83, v83
	v_fmac_f32_e32 v149, v82, v82
	v_fmac_f32_e32 v149, v84, v84
	v_fmac_f32_e32 v149, v85, v85
	s_waitcnt vmcnt(0)
	v_mov_b32_e32 v150, v79
	v_mov_b32_e32 v151, v75
	v_add_f32_e32 v152, v148, v149
	v_mov_b32_e32 v148, v78
	v_mov_b32_e32 v149, v74
	v_pk_mul_f32 v[150:151], v[150:151], v[150:151]
	s_nop 0
	v_pk_fma_f32 v[148:149], v[148:149], v[148:149], v[150:151]
	v_mov_b32_e32 v150, v80
	v_mov_b32_e32 v151, v76
	v_pk_fma_f32 v[148:149], v[150:151], v[150:151], v[148:149]
	v_mov_b32_e32 v150, v81
	v_mov_b32_e32 v151, v77
	v_pk_fma_f32 v[148:149], v[150:151], v[150:151], v[148:149]
	v_mov_b32_e32 v150, v71
	v_add_f32_e32 v148, v152, v148
	v_mov_b32_e32 v151, v67
	v_add_f32_e32 v152, v148, v149
	v_mov_b32_e32 v148, v70
	v_mov_b32_e32 v149, v66
	v_pk_mul_f32 v[150:151], v[150:151], v[150:151]
	s_nop 0
	v_pk_fma_f32 v[148:149], v[148:149], v[148:149], v[150:151]
	v_mov_b32_e32 v150, v72
	v_mov_b32_e32 v151, v68
	v_pk_fma_f32 v[148:149], v[150:151], v[150:151], v[148:149]
	v_mov_b32_e32 v150, v73
	v_mov_b32_e32 v151, v69
	v_pk_fma_f32 v[148:149], v[150:151], v[150:151], v[148:149]
	s_nop 0
	v_add_f32_e32 v148, v152, v148
	v_add_f32_e32 v148, v148, v149
	s_waitcnt lgkmcnt(0)
	s_nop 1
	v_add_f32_dpp v148, v148, v148 quad_perm:[1,0,3,2] row_mask:0xf bank_mask:0xf
	s_nop 1
	v_add_f32_dpp v148, v148, v148 quad_perm:[2,3,0,1] row_mask:0xf bank_mask:0xf
	s_nop 1
	v_add_f32_dpp v148, v148, v148 row_half_mirror row_mask:0xf bank_mask:0xf
	s_nop 1
	v_add_f32_dpp v148, v148, v148 row_mirror row_mask:0xf bank_mask:0xf
	v_mov_b32_e32 v149, v148
	s_nop 1
	v_permlane16_swap_b32 v148, v149
	v_add_f32_e32 v148, v148, v149
	v_mov_b32_e32 v149, v148
	s_nop 1
	v_permlane32_swap_b32 v148, v149
	v_add_f32_e32 v148, v148, v149
	v_fmamk_f32 v148, v148, 0x3a000000, v147
	v_mul_f32_e32 v149, 0x4b800000, v148
	v_cmp_gt_f32_e32 vcc, s25, v148
	s_nop 1
	v_cndmask_b32_e32 v148, v148, v149, vcc
	v_rsq_f32_e32 v148, v148
	s_nop 0
	v_mul_f32_e32 v149, 0x45800000, v148
	v_cndmask_b32_e32 v148, v148, v149, vcc
	v_pk_mul_f32 v[150:151], v[148:149], v[94:95] op_sel_hi:[0,1]
	v_pk_mul_f32 v[94:95], v[148:149], v[96:97] op_sel_hi:[0,1]
	v_pk_fma_f32 v[94:95], v[94:95], v[100:101], v[4:5]
	v_pk_fma_f32 v[96:97], v[150:151], v[102:103], v[2:3]
	v_max_f32_e64 v149, |v94|, |v95|
	v_max3_f32 v149, |v96|, |v97|, v149
	v_pk_mul_f32 v[150:151], v[148:149], v[90:91] op_sel_hi:[0,1]
	v_pk_mul_f32 v[90:91], v[148:149], v[92:93] op_sel_hi:[0,1]
	v_pk_fma_f32 v[90:91], v[90:91], v[104:105], v[8:9]
	v_pk_fma_f32 v[92:93], v[150:151], v[106:107], v[6:7]
	v_max_f32_e64 v150, |v90|, |v91|
	v_max3_f32 v150, |v92|, |v93|, v150
	v_max3_f32 v149, v149, 0, v150
	v_pk_mul_f32 v[150:151], v[148:149], v[86:87] op_sel_hi:[0,1]
	v_pk_mul_f32 v[86:87], v[148:149], v[88:89] op_sel_hi:[0,1]
	v_pk_fma_f32 v[86:87], v[86:87], v[108:109], v[12:13]
	v_pk_fma_f32 v[88:89], v[150:151], v[110:111], v[10:11]
	v_max_f32_e64 v150, |v86|, |v87|
	v_max3_f32 v152, |v88|, |v89|, v150
	v_pk_mul_f32 v[150:151], v[148:149], v[82:83] op_sel_hi:[0,1]
	v_pk_mul_f32 v[82:83], v[148:149], v[84:85] op_sel_hi:[0,1]
	v_pk_fma_f32 v[82:83], v[82:83], v[112:113], v[16:17]
	v_pk_fma_f32 v[84:85], v[150:151], v[114:115], v[14:15]
	v_max_f32_e64 v150, |v82|, |v83|
	v_max3_f32 v150, |v84|, |v85|, v150
	v_max3_f32 v149, v149, v152, v150
	v_pk_mul_f32 v[150:151], v[148:149], v[78:79] op_sel_hi:[0,1]
	v_pk_mul_f32 v[78:79], v[148:149], v[80:81] op_sel_hi:[0,1]
	v_pk_fma_f32 v[78:79], v[78:79], v[116:117], v[20:21]
	v_pk_fma_f32 v[80:81], v[150:151], v[118:119], v[18:19]
	v_max_f32_e64 v150, |v78|, |v79|
	v_max3_f32 v152, |v80|, |v81|, v150
	v_pk_mul_f32 v[150:151], v[148:149], v[74:75] op_sel_hi:[0,1]
	v_pk_mul_f32 v[74:75], v[148:149], v[76:77] op_sel_hi:[0,1]
	v_pk_fma_f32 v[74:75], v[74:75], v[120:121], v[24:25]
	v_pk_fma_f32 v[76:77], v[150:151], v[122:123], v[22:23]
	v_max_f32_e64 v150, |v74|, |v75|
	v_max3_f32 v150, |v76|, |v77|, v150
	v_max3_f32 v149, v149, v152, v150
	v_pk_mul_f32 v[150:151], v[148:149], v[70:71] op_sel_hi:[0,1]
	v_pk_mul_f32 v[70:71], v[148:149], v[72:73] op_sel_hi:[0,1]
	v_pk_fma_f32 v[70:71], v[70:71], v[124:125], v[28:29]
	v_pk_fma_f32 v[72:73], v[150:151], v[126:127], v[26:27]
	v_max_f32_e64 v150, |v70|, |v71|
	v_max3_f32 v152, |v72|, |v73|, v150
	v_pk_mul_f32 v[150:151], v[148:149], v[66:67] op_sel_hi:[0,1]
	v_pk_mul_f32 v[66:67], v[148:149], v[68:69] op_sel_hi:[0,1]
	v_pk_fma_f32 v[66:67], v[66:67], v[128:129], v[32:33]
	v_pk_fma_f32 v[68:69], v[150:151], v[130:131], v[30:31]
	v_max_f32_e64 v148, |v66|, |v67|
	v_max3_f32 v148, |v68|, |v69|, v148
	v_max3_f32 v148, v149, v152, v148
	s_waitcnt lgkmcnt(0)
	s_nop 1
	v_max_f32_dpp v148, v148, v148 quad_perm:[1,0,3,2] row_mask:0xf bank_mask:0xf
	s_nop 1
	v_max_f32_dpp v148, v148, v148 quad_perm:[2,3,0,1] row_mask:0xf bank_mask:0xf
	s_nop 1
	v_max_f32_dpp v148, v148, v148 row_half_mirror row_mask:0xf bank_mask:0xf
	s_nop 1
	v_max_f32_dpp v148, v148, v148 row_mirror row_mask:0xf bank_mask:0xf
	v_mov_b32_e32 v149, v148
	s_nop 1
	v_permlane16_swap_b32 v148, v149
	v_max_f32_e32 v148, v148, v149
	v_mov_b32_e32 v149, v148
	s_nop 1
	v_permlane32_swap_b32 v148, v149
	v_max_f32_e32 v148, v148, v149
	v_cmp_neq_f32_e32 vcc, 0, v148
	s_nop 1
	v_cndmask_b32_e32 v148, 1.0, v148, vcc
	s_and_saveexec_b64 s[22:23], s[4:5]
	s_cbranch_execz .LBB0_230
	s_add_u32 s34, s8, s3
	s_addc_u32 s35, s9, s24
	v_mul_f32_e32 v149, 0x3c010204, v148
	global_store_dword v165, v149, s[34:35]
	s_branch .LBB0_230
; __global__ void __launch_bounds__(NWAVES * 64, 2) fwd_kernel(Args a_unused) {
;     ...
;         if (gw < NCTX) {
;             const int m = gw; const float* xr = A->ctx + (size_t)m * D + 4 * lane; f32x4 v[8]; float ss = 0.f;
; #pragma unroll
;             for (int j = 0; j < 8; ++j) { v[j] = *(const f32x4*)(xr + 256 * j); ss += v[j][0] * v[j][0] + v[j][1] * v[j][1] + v[j][2] * v[j][2] + v[j][3] * v[j][3]; }
;             const float rstd = rsqrtf(wave_sum(ss) * (1.0f / D) + EPS);
.LBB0_235:
	s_cmpk_lt_i32 s58, 0x100
	s_cbranch_scc0 .LBB0_239
	s_load_dwordx2 s[14:15], s[10:11], 0x10
	s_load_dwordx2 s[4:5], s[10:11], 0x20
	s_lshl_b64 s[12:13], s[12:13], 2
	v_mov_b32_e32 v99, 0
	s_movk_i32 s3, 0x1000
	s_waitcnt lgkmcnt(0)
	s_add_u32 s12, s14, s12
	s_addc_u32 s13, s15, s13
	v_lshl_add_u64 v[2:3], s[12:13], 0, v[98:99]
	v_add_co_u32_e32 v34, vcc, s3, v2
	global_load_dwordx4 v[22:25], v98, s[12:13]
	global_load_dwordx4 v[18:21], v98, s[12:13] offset:1024
	global_load_dwordx4 v[14:17], v98, s[12:13] offset:2048
	global_load_dwordx4 v[10:13], v98, s[12:13] offset:3072
	v_addc_co_u32_e32 v35, vcc, 0, v3, vcc
	global_load_dwordx4 v[26:29], v[34:35], off
	global_load_dwordx4 v[2:5], v[34:35], off offset:1024
	global_load_dwordx4 v[30:33], v[34:35], off offset:2048
	global_load_dwordx4 v[6:9], v[34:35], off offset:3072
	v_mbcnt_lo_u32_b32 v34, -1, 0
	s_waitcnt vmcnt(13)
	v_mbcnt_hi_u32_b32 v106, -1, v34
	v_and_b32_e32 v34, 64, v106
	v_xor_b32_e32 v35, 1, v106
	v_add_u32_e32 v108, 64, v34
	v_cmp_lt_i32_e32 vcc, v35, v108
	v_xor_b32_e32 v36, 2, v106
	v_xor_b32_e32 v86, 4, v106
	v_cndmask_b32_e32 v34, v106, v35, vcc
	v_lshlrev_b32_e32 v131, 2, v34
	v_cmp_lt_i32_e32 vcc, v36, v108
	s_add_u32 s12, s8, 0x10c000
	v_xor_b32_e32 v87, 8, v106
	v_cndmask_b32_e32 v88, v106, v36, vcc
	v_lshlrev_b32_e32 v134, 2, v88
	v_cmp_lt_i32_e32 vcc, v86, v108
	s_addc_u32 s13, s9, 0
	s_add_u32 s14, s8, 0x10e000
	global_load_dwordx4 v[34:37], v98, s[4:5]
	global_load_dwordx4 v[38:41], v98, s[4:5] offset:1024
	global_load_dwordx4 v[42:45], v98, s[4:5] offset:2048
	s_addc_u32 s15, s9, 0
	global_load_dwordx4 v[46:49], v98, s[14:15]
	global_load_dwordx4 v[50:53], v98, s[12:13]
	global_load_dwordx4 v[54:57], v140, s[14:15]
	global_load_dwordx4 v[58:61], v140, s[12:13]
	global_load_dwordx4 v[62:65], v141, s[14:15]
	global_load_dwordx4 v[66:69], v141, s[12:13]
	v_xor_b32_e32 v94, 16, v106
	v_xor_b32_e32 v107, 32, v106
	s_waitcnt vmcnt(19)
	v_mov_b32_e32 v118, 0x358637bd
	s_mov_b32 s3, 0x800000
	s_waitcnt vmcnt(16)
	v_mul_f32_e32 v89, v23, v23
	s_waitcnt vmcnt(15)
	v_mul_f32_e32 v90, v19, v19
	s_waitcnt vmcnt(14)
	v_mul_f32_e32 v91, v15, v15
	v_fmac_f32_e32 v89, v22, v22
	v_fmac_f32_e32 v90, v18, v18
	s_waitcnt vmcnt(13)
	v_mul_f32_e32 v92, v11, v11
	v_fmac_f32_e32 v91, v14, v14
	v_fmac_f32_e32 v89, v24, v24
	v_fmac_f32_e32 v90, v20, v20
	s_waitcnt vmcnt(12)
	v_mov_b32_e32 v72, v27
	s_waitcnt vmcnt(11)
	v_mov_b32_e32 v73, v3
	v_fmac_f32_e32 v92, v10, v10
	v_fmac_f32_e32 v91, v16, v16
	v_mov_b32_e32 v70, v26
	v_mov_b32_e32 v71, v2
	s_waitcnt vmcnt(10)
	v_mov_b32_e32 v80, v31
	s_waitcnt vmcnt(9)
	v_mov_b32_e32 v81, v7
	v_fmac_f32_e32 v89, v25, v25
	v_fmac_f32_e32 v90, v21, v21
	v_pk_mul_f32 v[72:73], v[72:73], v[72:73]
	v_fmac_f32_e32 v92, v12, v12
	v_mov_b32_e32 v74, v28
	v_mov_b32_e32 v75, v4
	v_mov_b32_e32 v78, v30
	v_mov_b32_e32 v79, v6
	v_fmac_f32_e32 v91, v17, v17
	v_pk_mul_f32 v[80:81], v[80:81], v[80:81]
	v_add_f32_e32 v89, v89, v90
	v_pk_fma_f32 v[70:71], v[70:71], v[70:71], v[72:73]
	v_mov_b32_e32 v76, v29
	v_mov_b32_e32 v77, v5
	v_fmac_f32_e32 v92, v13, v13
	v_pk_fma_f32 v[72:73], v[78:79], v[78:79], v[80:81]
	v_add_f32_e32 v78, v89, v91
	v_pk_fma_f32 v[70:71], v[74:75], v[74:75], v[70:71]
	v_mov_b32_e32 v82, v32
	v_mov_b32_e32 v83, v8
	v_add_f32_e32 v74, v78, v92
	v_pk_fma_f32 v[70:71], v[76:77], v[76:77], v[70:71]
	v_mov_b32_e32 v84, v33
	v_mov_b32_e32 v85, v9
	v_pk_fma_f32 v[72:73], v[82:83], v[82:83], v[72:73]
	v_add_f32_e32 v70, v74, v70
	v_pk_fma_f32 v[72:73], v[84:85], v[84:85], v[72:73]
	v_add_f32_e32 v70, v70, v71
	v_add_f32_e32 v70, v70, v72
	v_add_f32_e32 v82, v70, v73
	ds_bpermute_b32 v83, v131, v82
	global_load_dwordx4 v[70:73], v139, s[14:15]
	global_load_dwordx4 v[74:77], v98, s[4:5] offset:3072
	global_load_dwordx4 v[78:81], v139, s[12:13]
	s_waitcnt vmcnt(8)
	v_pk_add_f32 v[46:47], v[46:47], 1.0 op_sel_hi:[1,0]
	s_waitcnt lgkmcnt(0)
	v_add_f32_e32 v88, v82, v83
	ds_bpermute_b32 v89, v134, v88
	v_cndmask_b32_e32 v82, v106, v86, vcc
	v_lshlrev_b32_e32 v135, 2, v82
	v_cmp_lt_i32_e32 vcc, v87, v108
	global_load_dwordx4 v[82:85], v138, s[14:15]
	s_waitcnt lgkmcnt(0)
	v_add_f32_e32 v95, v88, v89
	ds_bpermute_b32 v96, v135, v95
	v_cndmask_b32_e32 v90, v106, v87, vcc
	v_lshlrev_b32_e32 v139, 2, v90
	v_cmp_lt_i32_e32 vcc, v94, v108
	global_load_dwordx4 v[86:89], v138, s[4:5]
	global_load_dwordx4 v[90:93], v138, s[12:13]
	s_waitcnt lgkmcnt(0)
	v_add_f32_e32 v102, v95, v96
	ds_bpermute_b32 v103, v139, v102
	v_cndmask_b32_e32 v94, v106, v94, vcc
	v_lshlrev_b32_e32 v138, 2, v94
	v_cmp_lt_i32_e32 vcc, v107, v108
	global_load_dwordx4 v[94:97], v137, s[14:15]
	global_load_dwordx4 v[98:101], v137, s[4:5]
	s_waitcnt lgkmcnt(0)
	v_add_f32_e32 v109, v102, v103
	ds_bpermute_b32 v110, v138, v109
	v_cndmask_b32_e32 v106, v106, v107, vcc
	global_load_dwordx4 v[102:105], v137, s[12:13]
	v_lshlrev_b32_e32 v137, 2, v106
	v_pk_mul_f32 v[34:35], v[34:35], v[46:47]
	s_waitcnt lgkmcnt(0)
	v_add_f32_e32 v119, v109, v110
	ds_bpermute_b32 v120, v137, v119
	global_load_dwordx4 v[106:109], v136, s[14:15]
	global_load_dwordx4 v[110:113], v136, s[4:5]
	global_load_dwordx4 v[114:117], v136, s[12:13]
	s_waitcnt lgkmcnt(0)
; __global__ void __launch_bounds__(NWAVES * 64, 2) fwd_kernel(Args a_unused) {
;     ...
;             const float rstd = rsqrtf(wave_sum(ss) * (1.0f / D) + EPS);
;             float am = 0.f;
; #pragma unroll
;             for (int j = 0; j < 8; ++j) { const int k = 4 * lane + 256 * j; const f32x4 g = *(const f32x4*)(A->norm_mix_g + k), s1 = *(const f32x4*)(modc + 2048 + k), s0 = *(const f32x4*)(modc + k);
;                 v[j] = v[j] * rstd * (g * (1.0f + s1)) + s0; am = fmaxf(am, fmaxf(fmaxf(fabsf(v[j][0]), fabsf(v[j][1])), fmaxf(fabsf(v[j][2]), fabsf(v[j][3])))); }
; #pragma unroll
;             for (int o = 1; o < 64; o <<= 1) am = fmaxf(am, __shfl_xor(am, o));
;             if (am == 0.f) am = 1.f;
;             const float qi = 127.0f / am;
;             if (lane == 0) ((float*)(ws + WS_CS + CS_HROW))[NTOK + m] = am * (1.0f / 127.0f);
;             unsigned* hq = (unsigned*)((signed char*)(ws + WS_H) + (size_t)(NTOK + m) * D + 4 * lane);
; #pragma unroll
;             for (int j = 0; j < 8; ++j) hq[64 * j] = q8x4(v[j][0], v[j][1], v[j][2], v[j][3], qi);
	v_add_f32_e32 v119, v119, v120
	v_fmac_f32_e32 v118, 0x3a000000, v119
	v_mul_f32_e32 v119, 0x4b800000, v118
	v_cmp_gt_f32_e32 vcc, s3, v118
	s_nop 1
	v_cndmask_b32_e32 v118, v118, v119, vcc
	v_rsq_f32_e32 v126, v118
	global_load_dwordx4 v[118:121], v1, s[14:15]
	global_load_dwordx4 v[122:125], v1, s[4:5]
	v_mul_f32_e32 v127, 0x45800000, v126
	v_cndmask_b32_e32 v130, v126, v127, vcc
	global_load_dwordx4 v[126:129], v1, s[12:13]
	v_pk_mul_f32 v[132:133], v[130:131], v[22:23] op_sel_hi:[0,1]
	v_pk_mul_f32 v[22:23], v[130:131], v[24:25] op_sel_hi:[0,1]
	v_pk_add_f32 v[24:25], v[48:49], 1.0 op_sel_hi:[1,0]
	s_nop 0
	v_pk_mul_f32 v[24:25], v[36:37], v[24:25]
	s_waitcnt vmcnt(18)
	v_pk_add_f32 v[36:37], v[54:55], 1.0 op_sel_hi:[1,0]
	v_pk_fma_f32 v[22:23], v[24:25], v[22:23], v[52:53]
	v_pk_fma_f32 v[24:25], v[34:35], v[132:133], v[50:51]
	v_pk_mul_f32 v[34:35], v[130:131], v[18:19] op_sel_hi:[0,1]
	v_pk_mul_f32 v[18:19], v[130:131], v[20:21] op_sel_hi:[0,1]
	v_pk_add_f32 v[20:21], v[56:57], 1.0 op_sel_hi:[1,0]
	v_pk_mul_f32 v[36:37], v[38:39], v[36:37]
	v_pk_mul_f32 v[20:21], v[40:41], v[20:21]
	v_max_f32_e64 v1, |v22|, |v23|
	s_waitcnt vmcnt(17)
	v_pk_fma_f32 v[18:19], v[20:21], v[18:19], v[60:61]
	v_pk_fma_f32 v[20:21], v[36:37], v[34:35], v[58:59]
	v_max_f32_e64 v34, |v18|, |v19|
	v_max3_f32 v1, |v24|, |v25|, v1
	v_max3_f32 v34, |v20|, |v21|, v34
	v_max3_f32 v1, v1, 0, v34
	v_pk_mul_f32 v[34:35], v[130:131], v[14:15] op_sel_hi:[0,1]
	v_pk_mul_f32 v[14:15], v[130:131], v[16:17] op_sel_hi:[0,1]
	s_waitcnt vmcnt(16)
	v_pk_add_f32 v[16:17], v[64:65], 1.0 op_sel_hi:[1,0]
	v_pk_add_f32 v[36:37], v[62:63], 1.0 op_sel_hi:[1,0]
	v_pk_mul_f32 v[16:17], v[44:45], v[16:17]
	v_pk_mul_f32 v[36:37], v[42:43], v[36:37]
	s_waitcnt vmcnt(15)
	v_pk_fma_f32 v[14:15], v[16:17], v[14:15], v[68:69]
	v_pk_fma_f32 v[16:17], v[36:37], v[34:35], v[66:67]
	v_max_f32_e64 v34, |v14|, |v15|
	v_max3_f32 v38, |v16|, |v17|, v34
	v_pk_mul_f32 v[34:35], v[130:131], v[10:11] op_sel_hi:[0,1]
	v_pk_mul_f32 v[10:11], v[130:131], v[12:13] op_sel_hi:[0,1]
	s_waitcnt vmcnt(14)
	v_pk_add_f32 v[12:13], v[72:73], 1.0 op_sel_hi:[1,0]
	v_pk_add_f32 v[36:37], v[70:71], 1.0 op_sel_hi:[1,0]
	s_waitcnt vmcnt(13)
	v_pk_mul_f32 v[12:13], v[76:77], v[12:13]
	v_pk_mul_f32 v[36:37], v[74:75], v[36:37]
	s_waitcnt vmcnt(12)
	v_pk_fma_f32 v[10:11], v[12:13], v[10:11], v[80:81]
	v_pk_fma_f32 v[12:13], v[36:37], v[34:35], v[78:79]
	v_max_f32_e64 v34, |v10|, |v11|
	v_max3_f32 v34, |v12|, |v13|, v34
	v_max3_f32 v1, v1, v38, v34
	v_pk_mul_f32 v[34:35], v[130:131], v[26:27] op_sel_hi:[0,1]
	v_pk_mul_f32 v[26:27], v[130:131], v[28:29] op_sel_hi:[0,1]
	s_waitcnt vmcnt(11)
	v_pk_add_f32 v[28:29], v[84:85], 1.0 op_sel_hi:[1,0]
	v_pk_add_f32 v[36:37], v[82:83], 1.0 op_sel_hi:[1,0]
	s_waitcnt vmcnt(10)
	v_pk_mul_f32 v[28:29], v[88:89], v[28:29]
	v_pk_mul_f32 v[36:37], v[86:87], v[36:37]
	s_waitcnt vmcnt(9)
	v_pk_fma_f32 v[26:27], v[28:29], v[26:27], v[92:93]
	v_pk_fma_f32 v[28:29], v[36:37], v[34:35], v[90:91]
	v_max_f32_e64 v34, |v26|, |v27|
	v_max3_f32 v38, |v28|, |v29|, v34
	v_pk_mul_f32 v[34:35], v[130:131], v[2:3] op_sel_hi:[0,1]
	v_pk_mul_f32 v[2:3], v[130:131], v[4:5] op_sel_hi:[0,1]
	s_waitcnt vmcnt(8)
	v_pk_add_f32 v[4:5], v[96:97], 1.0 op_sel_hi:[1,0]
	v_pk_add_f32 v[36:37], v[94:95], 1.0 op_sel_hi:[1,0]
	s_waitcnt vmcnt(7)
	v_pk_mul_f32 v[4:5], v[100:101], v[4:5]
	v_pk_mul_f32 v[36:37], v[98:99], v[36:37]
	s_waitcnt vmcnt(6)
	v_pk_fma_f32 v[2:3], v[4:5], v[2:3], v[104:105]
	v_pk_fma_f32 v[4:5], v[36:37], v[34:35], v[102:103]
	v_max_f32_e64 v34, |v2|, |v3|
	v_max3_f32 v34, |v4|, |v5|, v34
	v_max3_f32 v1, v1, v38, v34
	v_pk_mul_f32 v[34:35], v[130:131], v[30:31] op_sel_hi:[0,1]
	v_pk_mul_f32 v[30:31], v[130:131], v[32:33] op_sel_hi:[0,1]
	s_waitcnt vmcnt(5)
	v_pk_add_f32 v[32:33], v[108:109], 1.0 op_sel_hi:[1,0]
	v_pk_add_f32 v[36:37], v[106:107], 1.0 op_sel_hi:[1,0]
	s_waitcnt vmcnt(4)
	v_pk_mul_f32 v[32:33], v[112:113], v[32:33]
	v_pk_mul_f32 v[36:37], v[110:111], v[36:37]
	s_waitcnt vmcnt(3)
	v_pk_fma_f32 v[30:31], v[32:33], v[30:31], v[116:117]
	v_pk_fma_f32 v[32:33], v[36:37], v[34:35], v[114:115]
	v_max_f32_e64 v34, |v30|, |v31|
	v_max3_f32 v38, |v32|, |v33|, v34
	v_pk_mul_f32 v[34:35], v[130:131], v[6:7] op_sel_hi:[0,1]
	v_pk_mul_f32 v[6:7], v[130:131], v[8:9] op_sel_hi:[0,1]
	s_waitcnt vmcnt(2)
	v_pk_add_f32 v[8:9], v[120:121], 1.0 op_sel_hi:[1,0]
	v_pk_add_f32 v[36:37], v[118:119], 1.0 op_sel_hi:[1,0]
	s_waitcnt vmcnt(1)
	v_pk_mul_f32 v[8:9], v[124:125], v[8:9]
	v_pk_mul_f32 v[36:37], v[122:123], v[36:37]
	s_waitcnt vmcnt(0)
	v_pk_fma_f32 v[6:7], v[8:9], v[6:7], v[128:129]
	v_pk_fma_f32 v[8:9], v[36:37], v[34:35], v[126:127]
	v_max_f32_e64 v34, |v6|, |v7|
	v_max3_f32 v34, |v8|, |v9|, v34
	v_max3_f32 v1, v1, v38, v34
	s_waitcnt lgkmcnt(0)
	s_nop 1
	v_max_f32_dpp v1, v1, v1 quad_perm:[1,0,3,2] row_mask:0xf bank_mask:0xf
	s_nop 1
	v_max_f32_dpp v1, v1, v1 quad_perm:[2,3,0,1] row_mask:0xf bank_mask:0xf
	s_nop 1
	v_max_f32_dpp v1, v1, v1 row_half_mirror row_mask:0xf bank_mask:0xf
	s_nop 1
	v_max_f32_dpp v1, v1, v1 row_mirror row_mask:0xf bank_mask:0xf
	v_mov_b32_e32 v34, v1
	s_nop 1
	v_permlane16_swap_b32 v1, v34
	v_max_f32_e32 v1, v1, v34
	v_mov_b32_e32 v34, v1
	s_nop 1
	v_permlane32_swap_b32 v1, v34
	v_max_f32_e32 v1, v1, v34
	v_cmp_neq_f32_e32 vcc, 0, v1
	s_nop 1
	v_cndmask_b32_e32 v1, 1.0, v1, vcc
	v_cmp_eq_u32_e32 vcc, 0, v162
	s_and_saveexec_b64 s[4:5], vcc
	s_cbranch_execz .LBB0_238
	s_lshl_b64 s[12:13], s[58:59], 2
	s_add_u32 s12, s8, s12
	s_addc_u32 s13, s9, s13
	v_mul_f32_e32 v34, 0x3c010204, v1
	v_mov_b32_e32 v35, 0xffc000
	global_store_dword v35, v34, s[12:13]

; DI float bflo(unsigned w) { return __uint_as_float(w << 16); }
; DI float bfhi(unsigned w) { return __uint_as_float(w & 0xffff0000u); }
; __global__ void __launch_bounds__(NWAVES * 64, 2) fwd_kernel(Args a_unused) {
;     ...
;               float am = 0.f;
; #pragma unroll
;               for (int j = 0; j < 8; ++j) am = fmaxf(am, fmaxf(fmaxf(fabsf(bflo(v[j][0])), fabsf(bfhi(v[j][0]))), fmaxf(fabsf(bflo(v[j][1])), fabsf(bfhi(v[j][1])))));
; #pragma unroll
;               for (int o = 1; o < 64; o <<= 1) am = fmaxf(am, __shfl_xor(am, o));
;               if (!(am > 0.f)) am = 1.f;
;               const float qi = 127.0f / am;
;               if (lane == 0) ((float*)(ws + WS_DLOG + DL_MRS))[m] = am * (1.0f / 127.0f);
.LBB0_1561:
	s_waitcnt vmcnt(3)
	v_lshlrev_b32_e32 v58, 16, v39
	v_and_b32_e32 v59, 0xffff0000, v39
	v_lshlrev_b32_e32 v56, 16, v38
	v_and_b32_e32 v57, 0xffff0000, v38
	v_max_f32_e64 v38, |v59|, |v59|
	v_max_f32_e64 v39, |v58|, |v58|
	v_max_f32_e32 v38, v39, v38
	v_lshlrev_b32_e32 v39, 16, v37
	v_and_b32_e32 v37, 0xffff0000, v37
	v_max_f32_e64 v45, |v37|, |v37|
	v_max_f32_e64 v46, |v39|, |v39|
	v_max3_f32 v44, |v56|, |v57|, v38
	v_lshlrev_b32_e32 v38, 16, v36
	v_and_b32_e32 v36, 0xffff0000, v36
	v_max_f32_e32 v45, v46, v45
	v_max3_f32 v45, |v38|, |v36|, v45
	v_max3_f32 v48, v44, 0, v45
	v_lshlrev_b32_e32 v45, 16, v35
	v_and_b32_e32 v35, 0xffff0000, v35
	v_max_f32_e64 v46, |v35|, |v35|
	v_max_f32_e64 v47, |v45|, |v45|
	v_max_f32_e32 v46, v47, v46
	v_lshlrev_b32_e32 v47, 16, v33
	v_and_b32_e32 v33, 0xffff0000, v33
	v_lshlrev_b32_e32 v44, 16, v34
	v_and_b32_e32 v34, 0xffff0000, v34
	v_max_f32_e64 v50, |v33|, |v33|
	v_max_f32_e64 v51, |v47|, |v47|
	v_max3_f32 v49, |v44|, |v34|, v46
	v_lshlrev_b32_e32 v46, 16, v32
	v_and_b32_e32 v32, 0xffff0000, v32
	v_max_f32_e32 v50, v51, v50
	v_max3_f32 v50, |v46|, |v32|, v50
	v_max3_f32 v52, v48, v49, v50
	v_lshlrev_b32_e32 v49, 16, v31
	v_and_b32_e32 v31, 0xffff0000, v31
	v_max_f32_e64 v50, |v31|, |v31|
	v_max_f32_e64 v51, |v49|, |v49|
	v_max_f32_e32 v50, v51, v50
	s_waitcnt vmcnt(2)
	v_lshlrev_b32_e32 v51, 16, v29
	v_and_b32_e32 v29, 0xffff0000, v29
	v_lshlrev_b32_e32 v48, 16, v30
	v_and_b32_e32 v30, 0xffff0000, v30
	v_max_f32_e64 v54, |v29|, |v29|
	v_max_f32_e64 v55, |v51|, |v51|
	v_max3_f32 v53, |v48|, |v30|, v50
	v_lshlrev_b32_e32 v50, 16, v28
	v_and_b32_e32 v28, 0xffff0000, v28
	v_max_f32_e32 v54, v55, v54
	v_max3_f32 v54, |v50|, |v28|, v54
	v_max3_f32 v60, v52, v53, v54
	s_waitcnt vmcnt(1)
	v_lshlrev_b32_e32 v53, 16, v27
	v_and_b32_e32 v27, 0xffff0000, v27
	v_max_f32_e64 v54, |v27|, |v27|
	v_max_f32_e64 v55, |v53|, |v53|
	v_max_f32_e32 v54, v55, v54
	s_waitcnt vmcnt(0)
	v_lshlrev_b32_e32 v55, 16, v25
	v_and_b32_e32 v25, 0xffff0000, v25
	v_lshlrev_b32_e32 v52, 16, v26
	v_and_b32_e32 v26, 0xffff0000, v26
	v_max_f32_e64 v62, |v25|, |v25|
	v_max_f32_e64 v63, |v55|, |v55|
	v_max3_f32 v61, |v52|, |v26|, v54
	v_lshlrev_b32_e32 v54, 16, v24
	v_and_b32_e32 v24, 0xffff0000, v24
	v_max_f32_e32 v62, v63, v62
	v_max3_f32 v62, |v54|, |v24|, v62
	v_max3_f32 v60, v60, v61, v62
	s_waitcnt lgkmcnt(0)
	s_nop 1
	v_max_f32_dpp v60, v60, v60 quad_perm:[1,0,3,2] row_mask:0xf bank_mask:0xf
	s_nop 1
	v_max_f32_dpp v60, v60, v60 quad_perm:[2,3,0,1] row_mask:0xf bank_mask:0xf
	s_nop 1
	v_max_f32_dpp v60, v60, v60 row_half_mirror row_mask:0xf bank_mask:0xf
	s_nop 1
	v_max_f32_dpp v60, v60, v60 row_mirror row_mask:0xf bank_mask:0xf
	v_mov_b32_e32 v61, v60
	s_nop 1
	v_permlane16_swap_b32 v60, v61
	v_max_f32_e32 v60, v60, v61
	v_mov_b32_e32 v61, v60
	s_nop 1
	v_permlane32_swap_b32 v60, v61
	v_max_f32_e32 v60, v60, v61
	v_cmp_lt_f32_e32 vcc, 0, v60
	s_nop 1
	v_cndmask_b32_e32 v60, 1.0, v60, vcc
	s_and_saveexec_b64 s[20:21], s[4:5]
	s_cbranch_execz .LBB0_1558
	s_add_u32 s28, s8, s3
	s_addc_u32 s29, s9, s22
	v_mul_f32_e32 v61, 0x3c010204, v60
	global_store_dword v3, v61, s[28:29]
	s_branch .LBB0_1558

; DI float bflo(unsigned w) { return __uint_as_float(w << 16); }
; DI float bfhi(unsigned w) { return __uint_as_float(w & 0xffff0000u); }
; __global__ void __launch_bounds__(NWAVES * 64, 2) fwd_kernel(Args a_unused) {
;     ...
;             for (int q = 0; q < 2; ++q) { const int m = row0 + 2 * wave + q; const unsigned short* xr = X1 + (size_t)m * D + 4 * lane; f32x4 v[8]; float ss = 0.f;
; #pragma unroll
;                 for (int j = 0; j < 8; ++j) { const u32x2 w2 = *(const u32x2*)(xr + 256 * j); v[j] = (f32x4){bflo(w2[0]), bfhi(w2[0]), bflo(w2[1]), bfhi(w2[1])}; ss += v[j][0] * v[j][0] + v[j][1] * v[j][1] + v[j][2] * v[j][2] + v[j][3] * v[j][3]; }
;                 const float rstd = rsqrtf(wave_sum(ss) * (1.0f / D) + EPS);
;                 if (lane == 0) rsd[2 * wave + q] = rstd;
;                 float am = 0.f;
; #pragma unroll
;                 for (int j = 0; j < 8; ++j) { const int k = 4 * lane + 256 * j; const f32x4 g = *(const f32x4*)(A->norm_ffn_g + k), s1 = *(const f32x4*)(modl + 4 * 2048 + k), s0 = *(const f32x4*)(modl + 3 * 2048 + k);
;                     v[j] = v[j] * rstd * (g * (1.0f + s1)) + s0; am = fmaxf(am, fmaxf(fmaxf(fabsf(v[j][0]), fabsf(v[j][1])), fmaxf(fabsf(v[j][2]), fabsf(v[j][3])))); }
.LBB0_1863:
	s_add_i32 s6, s30, s36
	s_ashr_i32 s7, s6, 31
	s_lshl_b64 s[8:9], s[6:7], 12
	v_lshl_add_u64 v[130:131], v[134:135], 0, s[8:9]
	global_load_dwordx2 v[132:133], v[130:131], off
	global_load_dwordx2 v[194:195], v[130:131], off offset:512
	global_load_dwordx2 v[196:197], v[130:131], off offset:1024
	global_load_dwordx2 v[198:199], v[130:131], off offset:1536
	global_load_dwordx2 v[200:201], v[130:131], off offset:2560
	global_load_dwordx2 v[220:221], v[130:131], off offset:2048
	global_load_dwordx2 v[222:223], v[130:131], off offset:3584
	global_load_dwordx2 v[228:229], v[130:131], off offset:3072
	s_waitcnt vmcnt(7)
	v_and_b32_e32 v203, 0xffff0000, v132
	s_waitcnt vmcnt(6)
	v_and_b32_e32 v209, 0xffff0000, v194
	v_lshlrev_b32_e32 v202, 16, v132
	v_lshlrev_b32_e32 v208, 16, v194
	s_waitcnt vmcnt(5)
	v_and_b32_e32 v213, 0xffff0000, v196
	v_mul_f32_e32 v193, v203, v203
	v_mul_f32_e32 v206, v209, v209
	v_lshlrev_b32_e32 v204, 16, v133
	v_lshlrev_b32_e32 v210, 16, v195
	v_lshlrev_b32_e32 v212, 16, v196
	s_waitcnt vmcnt(4)
	v_and_b32_e32 v217, 0xffff0000, v198
	s_waitcnt vmcnt(0)
	v_lshlrev_b32_e32 v194, 16, v228
	v_and_b32_e32 v196, 0xffff0000, v228
	v_mul_f32_e32 v228, v213, v213
	v_fmac_f32_e32 v193, v202, v202
	v_fmac_f32_e32 v206, v208, v208
	v_and_b32_e32 v205, 0xffff0000, v133
	v_and_b32_e32 v211, 0xffff0000, v195
	v_lshlrev_b32_e32 v214, 16, v197
	v_lshlrev_b32_e32 v216, 16, v198
	v_lshlrev_b32_e32 v131, 16, v200
	v_and_b32_e32 v133, 0xffff0000, v200
	v_and_b32_e32 v132, 0xffff0000, v220
	v_lshlrev_b32_e32 v198, 16, v229
	v_and_b32_e32 v200, 0xffff0000, v229
	v_mul_f32_e32 v229, v217, v217
	v_fmac_f32_e32 v228, v212, v212
	v_fmac_f32_e32 v193, v204, v204
	v_fmac_f32_e32 v206, v210, v210
	v_and_b32_e32 v215, 0xffff0000, v197
	v_lshlrev_b32_e32 v218, 16, v199
	v_lshlrev_b32_e32 v130, 16, v220
	v_lshlrev_b32_e32 v224, 16, v221
	v_and_b32_e32 v226, 0xffff0000, v221
	v_pk_mul_f32 v[220:221], v[132:133], v[132:133]
	v_fmac_f32_e32 v229, v216, v216
	v_fmac_f32_e32 v228, v214, v214
	v_fmac_f32_e32 v193, v205, v205
	v_fmac_f32_e32 v206, v211, v211
	v_and_b32_e32 v219, 0xffff0000, v199
	v_lshlrev_b32_e32 v225, 16, v201
	v_and_b32_e32 v197, 0xffff0000, v222
	v_pk_fma_f32 v[220:221], v[130:131], v[130:131], v[220:221]
	v_fmac_f32_e32 v229, v218, v218
	v_fmac_f32_e32 v228, v215, v215
	v_add_f32_e32 v193, v193, v206
	v_and_b32_e32 v227, 0xffff0000, v201
	v_lshlrev_b32_e32 v195, 16, v222
	v_lshlrev_b32_e32 v199, 16, v223
	v_and_b32_e32 v201, 0xffff0000, v223
	v_pk_mul_f32 v[222:223], v[196:197], v[196:197]
	v_pk_fma_f32 v[220:221], v[224:225], v[224:225], v[220:221]
	v_fmac_f32_e32 v229, v219, v219
	v_add_f32_e32 v193, v193, v228
	v_pk_fma_f32 v[222:223], v[194:195], v[194:195], v[222:223]
	v_pk_fma_f32 v[220:221], v[226:227], v[226:227], v[220:221]
	v_add_f32_e32 v193, v193, v229
	v_pk_fma_f32 v[222:223], v[198:199], v[198:199], v[222:223]
	v_add_f32_e32 v193, v193, v220
	v_pk_fma_f32 v[222:223], v[200:201], v[200:201], v[222:223]
	v_add_f32_e32 v193, v193, v221
	v_add_f32_e32 v193, v193, v222
	v_add_f32_e32 v193, v193, v223
	s_waitcnt lgkmcnt(0)
	s_nop 1
	v_add_f32_dpp v193, v193, v193 quad_perm:[1,0,3,2] row_mask:0xf bank_mask:0xf
	s_nop 1
	v_add_f32_dpp v193, v193, v193 quad_perm:[2,3,0,1] row_mask:0xf bank_mask:0xf
	s_nop 1
	v_add_f32_dpp v193, v193, v193 row_half_mirror row_mask:0xf bank_mask:0xf
	s_nop 1
	v_add_f32_dpp v193, v193, v193 row_mirror row_mask:0xf bank_mask:0xf
	v_mov_b32_e32 v206, v193
	s_nop 1
	v_permlane16_swap_b32 v193, v206
	v_add_f32_e32 v193, v193, v206
	v_mov_b32_e32 v206, v193
	s_nop 1
	v_permlane32_swap_b32 v193, v206
	v_add_f32_e32 v193, v193, v206
	v_fmamk_f32 v193, v193, 0x3a000000, v238
	v_mul_f32_e32 v206, 0x4b800000, v193
	v_cmp_gt_f32_e32 vcc, s39, v193
	s_nop 1
	v_cndmask_b32_e32 v193, v193, v206, vcc
	v_rsq_f32_e32 v193, v193
	s_nop 0
	v_mul_f32_e32 v206, 0x45800000, v193
	v_cndmask_b32_e32 v206, v193, v206, vcc
	s_and_saveexec_b64 s[8:9], s[4:5]
	v_mov_b32_e32 v193, s31
	ds_write_b32 v193, v206 offset:16384
	s_or_b64 exec, exec, s[8:9]
	global_load_dwordx4 v[220:223], v[144:145], off
	global_load_dwordx4 v[228:231], v[146:147], off
	global_load_dwordx4 v[242:245], v[148:149], off
	v_pk_mul_f32 v[246:247], v[206:207], v[202:203] op_sel_hi:[0,1]
	v_pk_mul_f32 v[202:203], v[206:207], v[204:205] op_sel_hi:[0,1]
	v_mov_b32_e32 v249, v226
	v_mov_b32_e32 v226, v225
	s_waitcnt vmcnt(1)
	v_pk_add_f32 v[204:205], v[230:231], 1.0 op_sel_hi:[1,0]
	v_pk_add_f32 v[228:229], v[228:229], 1.0 op_sel_hi:[1,0]
	v_pk_mul_f32 v[204:205], v[222:223], v[204:205]
	v_pk_mul_f32 v[220:221], v[220:221], v[228:229]
	s_waitcnt vmcnt(0)
	v_pk_fma_f32 v[202:203], v[204:205], v[202:203], v[244:245]
	v_pk_fma_f32 v[204:205], v[220:221], v[246:247], v[242:243]
	global_load_dwordx4 v[220:223], v[144:145], off offset:1024
	global_load_dwordx4 v[228:231], v[150:151], off
	global_load_dwordx4 v[242:245], v[152:153], off
	v_pk_mul_f32 v[246:247], v[206:207], v[208:209] op_sel_hi:[0,1]
	v_pk_mul_f32 v[208:209], v[206:207], v[210:211] op_sel_hi:[0,1]
	v_max_f32_e64 v193, |v202|, |v203|
	v_max3_f32 v193, |v204|, |v205|, v193
	s_waitcnt vmcnt(1)
	v_pk_add_f32 v[210:211], v[230:231], 1.0 op_sel_hi:[1,0]
	v_pk_add_f32 v[228:229], v[228:229], 1.0 op_sel_hi:[1,0]
	v_pk_mul_f32 v[210:211], v[222:223], v[210:211]
	v_pk_mul_f32 v[220:221], v[220:221], v[228:229]
	s_waitcnt vmcnt(0)
	v_pk_fma_f32 v[208:209], v[210:211], v[208:209], v[244:245]
	v_pk_fma_f32 v[210:211], v[220:221], v[246:247], v[242:243]
	v_max_f32_e64 v220, |v208|, |v209|
	v_max3_f32 v220, |v210|, |v211|, v220
	v_max3_f32 v193, v193, 0, v220
	global_load_dwordx4 v[220:223], v[144:145], off offset:2048
	global_load_dwordx4 v[228:231], v[154:155], off
	global_load_dwordx4 v[242:245], v[156:157], off
	v_pk_mul_f32 v[246:247], v[206:207], v[212:213] op_sel_hi:[0,1]
	v_pk_mul_f32 v[212:213], v[206:207], v[214:215] op_sel_hi:[0,1]
	s_waitcnt vmcnt(1)
; __global__ void __launch_bounds__(NWAVES * 64, 2) fwd_kernel(Args a_unused) {
;     ...
;                 float am = 0.f;
; #pragma unroll
;                 for (int j = 0; j < 8; ++j) { const int k = 4 * lane + 256 * j; const f32x4 g = *(const f32x4*)(A->norm_ffn_g + k), s1 = *(const f32x4*)(modl + 4 * 2048 + k), s0 = *(const f32x4*)(modl + 3 * 2048 + k);
;                     v[j] = v[j] * rstd * (g * (1.0f + s1)) + s0; am = fmaxf(am, fmaxf(fmaxf(fabsf(v[j][0]), fabsf(v[j][1])), fmaxf(fabsf(v[j][2]), fabsf(v[j][3])))); }
; #pragma unroll
;                 for (int o = 1; o < 64; o <<= 1) am = fmaxf(am, __shfl_xor(am, o));
;                 if (am == 0.f) am = 1.f;
;                 const float qi = 127.0f / am;
;                 if (lane == 0) ((float*)(ws + WS_CS + CS_ROW))[m] = am * (1.0f / 127.0f);
	v_pk_add_f32 v[214:215], v[230:231], 1.0 op_sel_hi:[1,0]
	v_pk_add_f32 v[228:229], v[228:229], 1.0 op_sel_hi:[1,0]
	v_pk_mul_f32 v[214:215], v[222:223], v[214:215]
	v_pk_mul_f32 v[220:221], v[220:221], v[228:229]
	s_waitcnt vmcnt(0)
	v_pk_fma_f32 v[212:213], v[214:215], v[212:213], v[244:245]
	v_pk_fma_f32 v[214:215], v[220:221], v[246:247], v[242:243]
	v_max_f32_e64 v220, |v212|, |v213|
	v_max3_f32 v248, |v214|, |v215|, v220
	global_load_dwordx4 v[220:223], v[144:145], off offset:3072
	global_load_dwordx4 v[228:231], v[158:159], off
	global_load_dwordx4 v[242:245], v[160:161], off
	v_pk_mul_f32 v[246:247], v[206:207], v[216:217] op_sel_hi:[0,1]
	v_pk_mul_f32 v[216:217], v[206:207], v[218:219] op_sel_hi:[0,1]
	s_waitcnt vmcnt(1)
	v_pk_add_f32 v[218:219], v[230:231], 1.0 op_sel_hi:[1,0]
	v_pk_add_f32 v[228:229], v[228:229], 1.0 op_sel_hi:[1,0]
	v_pk_mul_f32 v[218:219], v[222:223], v[218:219]
	v_pk_mul_f32 v[220:221], v[220:221], v[228:229]
	s_waitcnt vmcnt(0)
	v_pk_fma_f32 v[216:217], v[218:219], v[216:217], v[244:245]
	v_pk_fma_f32 v[218:219], v[220:221], v[246:247], v[242:243]
	v_max_f32_e64 v220, |v216|, |v217|
	v_max3_f32 v220, |v218|, |v219|, v220
	v_max3_f32 v193, v193, v248, v220
	global_load_dwordx4 v[220:223], v[168:169], off
	global_load_dwordx4 v[228:231], v[170:171], off
	global_load_dwordx4 v[242:245], v[172:173], off
	v_mov_b32_e32 v246, v130
	v_mov_b32_e32 v247, v132
	v_mov_b32_e32 v248, v224
	v_pk_mul_f32 v[246:247], v[206:207], v[246:247] op_sel_hi:[0,1]
	v_pk_mul_f32 v[248:249], v[206:207], v[248:249] op_sel_hi:[0,1]
	v_mov_b32_e32 v132, v131
	s_waitcnt vmcnt(1)
	v_pk_add_f32 v[230:231], v[230:231], 1.0 op_sel_hi:[1,0]
	v_pk_add_f32 v[228:229], v[228:229], 1.0 op_sel_hi:[1,0]
	v_pk_mul_f32 v[222:223], v[222:223], v[230:231]
	v_pk_mul_f32 v[228:229], v[220:221], v[228:229]
	s_waitcnt vmcnt(0)
	v_pk_fma_f32 v[220:221], v[222:223], v[248:249], v[244:245]
	v_pk_fma_f32 v[222:223], v[228:229], v[246:247], v[242:243]
	global_load_dwordx4 v[228:231], v[174:175], off
	global_load_dwordx4 v[242:245], v[176:177], off
	global_load_dwordx4 v[246:249], v[178:179], off
	v_max_f32_e64 v130, |v220|, |v221|
	v_max3_f32 v250, |v222|, |v223|, v130
	v_pk_mul_f32 v[130:131], v[206:207], v[132:133] op_sel_hi:[0,1]
	v_pk_mul_f32 v[132:133], v[206:207], v[226:227] op_sel_hi:[0,1]
	s_waitcnt vmcnt(1)
	v_pk_add_f32 v[224:225], v[244:245], 1.0 op_sel_hi:[1,0]
	v_pk_add_f32 v[226:227], v[242:243], 1.0 op_sel_hi:[1,0]
	v_pk_mul_f32 v[224:225], v[230:231], v[224:225]
	v_pk_mul_f32 v[226:227], v[228:229], v[226:227]
	s_waitcnt vmcnt(0)
	v_pk_fma_f32 v[224:225], v[224:225], v[132:133], v[248:249]
	v_pk_fma_f32 v[226:227], v[226:227], v[130:131], v[246:247]
	v_max_f32_e64 v130, |v224|, |v225|
	v_max3_f32 v130, |v226|, |v227|, v130
	v_max3_f32 v193, v193, v250, v130
	global_load_dwordx4 v[130:133], v[180:181], off
	global_load_dwordx4 v[228:231], v[182:183], off
	global_load_dwordx4 v[242:245], v[184:185], off
	v_mov_b32_e32 v248, v198
	v_mov_b32_e32 v249, v200
	v_mov_b32_e32 v246, v194
	v_mov_b32_e32 v247, v196
	v_pk_mul_f32 v[248:249], v[206:207], v[248:249] op_sel_hi:[0,1]
	v_pk_mul_f32 v[246:247], v[206:207], v[246:247] op_sel_hi:[0,1]
	v_mov_b32_e32 v196, v195
	v_mov_b32_e32 v200, v199
	v_pk_mul_f32 v[194:195], v[206:207], v[196:197] op_sel_hi:[0,1]
	v_pk_mul_f32 v[196:197], v[206:207], v[200:201] op_sel_hi:[0,1]
	s_waitcnt vmcnt(1)
	v_pk_add_f32 v[230:231], v[230:231], 1.0 op_sel_hi:[1,0]
	v_pk_add_f32 v[228:229], v[228:229], 1.0 op_sel_hi:[1,0]
	v_pk_mul_f32 v[132:133], v[132:133], v[230:231]
	v_pk_mul_f32 v[130:131], v[130:131], v[228:229]
	s_waitcnt vmcnt(0)
	v_pk_fma_f32 v[228:229], v[132:133], v[248:249], v[244:245]
	v_pk_fma_f32 v[230:231], v[130:131], v[246:247], v[242:243]
	v_max_f32_e64 v130, |v228|, |v229|
	v_max3_f32 v250, |v230|, |v231|, v130
	global_load_dwordx4 v[130:133], v[186:187], off
	global_load_dwordx4 v[242:245], v[188:189], off
	global_load_dwordx4 v[246:249], v[190:191], off
	s_waitcnt vmcnt(1)
	v_pk_add_f32 v[198:199], v[244:245], 1.0 op_sel_hi:[1,0]
	v_pk_add_f32 v[200:201], v[242:243], 1.0 op_sel_hi:[1,0]
	v_pk_mul_f32 v[132:133], v[132:133], v[198:199]
	v_pk_mul_f32 v[198:199], v[130:131], v[200:201]
	s_waitcnt vmcnt(0)
	v_pk_fma_f32 v[130:131], v[132:133], v[196:197], v[248:249]
	v_pk_fma_f32 v[132:133], v[198:199], v[194:195], v[246:247]
	v_max_f32_e64 v194, |v130|, |v131|
	v_max3_f32 v194, |v132|, |v133|, v194
	v_max3_f32 v193, v193, v250, v194
	s_waitcnt lgkmcnt(0)
	s_nop 1
	v_max_f32_dpp v193, v193, v193 quad_perm:[1,0,3,2] row_mask:0xf bank_mask:0xf
	s_nop 1
	v_max_f32_dpp v193, v193, v193 quad_perm:[2,3,0,1] row_mask:0xf bank_mask:0xf
	s_nop 1
	v_max_f32_dpp v193, v193, v193 row_half_mirror row_mask:0xf bank_mask:0xf
	s_nop 1
	v_max_f32_dpp v193, v193, v193 row_mirror row_mask:0xf bank_mask:0xf
	v_mov_b32_e32 v194, v193
	s_nop 1
	v_permlane16_swap_b32 v193, v194
	v_max_f32_e32 v193, v193, v194
	v_mov_b32_e32 v194, v193
	s_nop 1
	v_permlane32_swap_b32 v193, v194
	v_max_f32_e32 v193, v193, v194
	v_cmp_neq_f32_e32 vcc, 0, v193
	s_nop 1
	v_cndmask_b32_e32 v193, 1.0, v193, vcc
	s_and_saveexec_b64 s[8:9], s[4:5]
	s_cbranch_execz .LBB0_1867
	s_lshl_b64 s[10:11], s[6:7], 2
	s_add_u32 s10, s34, s10
	s_addc_u32 s11, s35, s11
	v_mul_f32_e32 v194, 0x3c010204, v193
	global_store_dword v165, v194, s[10:11]
; DI float bflo(unsigned w) { return __uint_as_float(w << 16); }
; DI float bfhi(unsigned w) { return __uint_as_float(w & 0xffff0000u); }
; __global__ void __launch_bounds__(NWAVES * 64, 2) fwd_kernel(Args a_unused) {
;     ...
;             for (int q = 0; q < 2; ++q) { const int m = row0 + 2 * wave + q; const unsigned short* xr = X1 + (size_t)m * D + 4 * lane; f32x4 v[8]; float ss = 0.f;
; #pragma unroll
;                 for (int j = 0; j < 8; ++j) { const u32x2 w2 = *(const u32x2*)(xr + 256 * j); v[j] = (f32x4){bflo(w2[0]), bfhi(w2[0]), bflo(w2[1]), bfhi(w2[1])}; ss += v[j][0] * v[j][0] + v[j][1] * v[j][1] + v[j][2] * v[j][2] + v[j][3] * v[j][3]; }
;     ...
;                 const float qi = 127.0f / am;
;                 if (lane == 0) ((float*)(ws + WS_CS + CS_ROW))[m] = am * (1.0f / 127.0f);
;                 unsigned* hq = (unsigned*)((signed char*)(ws + WS_H) + (size_t)m * D + 4 * lane);
; #pragma unroll
;                 for (int j = 0; j < 8; ++j) hq[64 * j] = q8x4(v[j][0], v[j][1], v[j][2], v[j][3], qi); }
.LBB0_1867:
	s_or_b64 exec, exec, s[8:9]
	v_div_scale_f32 v194, s[8:9], v193, v193, s42
	v_rcp_f32_e32 v195, v194
	s_lshl_b64 s[8:9], s[6:7], 11
	s_add_i32 s6, s6, 1
	s_ashr_i32 s7, s6, 31
	v_fma_f32 v196, -v194, v195, 1.0
	v_fmac_f32_e32 v195, v196, v195
	v_div_scale_f32 v196, vcc, s42, v193, s42
	v_mul_f32_e32 v197, v196, v195
	v_fma_f32 v198, -v194, v197, v196
	v_fmac_f32_e32 v197, v198, v195
	v_fma_f32 v194, -v194, v197, v196
	v_div_fmas_f32 v194, v194, v195, v197
	v_div_fixup_f32 v193, v194, v193, s42
	v_fmaak_f32 v196, v204, v193, 0x4b400000
	v_fmaak_f32 v197, v205, v193, 0x4b400000
	v_fmaak_f32 v198, v202, v193, 0x4b400000
	v_fmaak_f32 v199, v203, v193, 0x4b400000
	v_perm_b32 v198, v199, v198, s43
	v_perm_b32 v196, v197, v196, s43
	v_lshl_add_u64 v[194:195], v[136:137], 0, s[8:9]
	v_perm_b32 v196, v198, v196, s44
	global_store_dword v[194:195], v196, off
	v_fmaak_f32 v196, v210, v193, 0x4b400000
	v_fmaak_f32 v197, v211, v193, 0x4b400000
	v_fmaak_f32 v198, v208, v193, 0x4b400000
	v_fmaak_f32 v199, v209, v193, 0x4b400000
	v_perm_b32 v198, v199, v198, s43
	v_perm_b32 v196, v197, v196, s43
	v_perm_b32 v196, v198, v196, s44
	global_store_dword v[194:195], v196, off offset:256
	v_fmaak_f32 v196, v214, v193, 0x4b400000
	v_fmaak_f32 v197, v215, v193, 0x4b400000
	v_fmaak_f32 v198, v212, v193, 0x4b400000
	v_fmaak_f32 v199, v213, v193, 0x4b400000
	v_perm_b32 v198, v199, v198, s43
	v_perm_b32 v196, v197, v196, s43
	v_perm_b32 v196, v198, v196, s44
	global_store_dword v[194:195], v196, off offset:512
	v_fmaak_f32 v196, v218, v193, 0x4b400000
	v_fmaak_f32 v197, v219, v193, 0x4b400000
	v_fmaak_f32 v198, v216, v193, 0x4b400000
	v_fmaak_f32 v199, v217, v193, 0x4b400000
	v_perm_b32 v198, v199, v198, s43
	v_perm_b32 v196, v197, v196, s43
	v_perm_b32 v196, v198, v196, s44
	global_store_dword v[194:195], v196, off offset:768
	v_fmaak_f32 v196, v222, v193, 0x4b400000
	v_fmaak_f32 v197, v223, v193, 0x4b400000
	v_fmaak_f32 v198, v220, v193, 0x4b400000
	v_fmaak_f32 v199, v221, v193, 0x4b400000
	v_perm_b32 v198, v199, v198, s43
	v_perm_b32 v196, v197, v196, s43
	v_perm_b32 v196, v198, v196, s44
	global_store_dword v[194:195], v196, off offset:1024
	v_fmaak_f32 v196, v226, v193, 0x4b400000
	v_fmaak_f32 v197, v227, v193, 0x4b400000
	v_fmaak_f32 v198, v224, v193, 0x4b400000
	v_fmaak_f32 v199, v225, v193, 0x4b400000
	v_perm_b32 v198, v199, v198, s43
	v_perm_b32 v196, v197, v196, s43
	v_perm_b32 v196, v198, v196, s44
	global_store_dword v[194:195], v196, off offset:1280
	v_fmaak_f32 v196, v230, v193, 0x4b400000
	v_fmaak_f32 v197, v231, v193, 0x4b400000
	v_fmaak_f32 v198, v228, v193, 0x4b400000
	v_fmaak_f32 v199, v229, v193, 0x4b400000
	v_fmaak_f32 v132, v132, v193, 0x4b400000
	v_fmaak_f32 v133, v133, v193, 0x4b400000
	v_fmaak_f32 v130, v130, v193, 0x4b400000
	v_fmaak_f32 v131, v131, v193, 0x4b400000
	v_perm_b32 v198, v199, v198, s43
	v_perm_b32 v196, v197, v196, s43
	v_perm_b32 v130, v131, v130, s43
	v_perm_b32 v131, v133, v132, s43
	v_perm_b32 v196, v198, v196, s44
	v_perm_b32 v130, v130, v131, s44
	s_lshl_b64 s[8:9], s[6:7], 12
	global_store_dword v[194:195], v196, off offset:1536
	global_store_dword v[194:195], v130, off offset:1792
	v_lshl_add_u64 v[130:131], v[134:135], 0, s[8:9]
	global_load_dwordx2 v[132:133], v[130:131], off
	global_load_dwordx2 v[198:199], v[130:131], off offset:512
	global_load_dwordx2 v[200:201], v[130:131], off offset:1024
	global_load_dwordx2 v[202:203], v[130:131], off offset:1536
	global_load_dwordx2 v[204:205], v[130:131], off offset:2560
	global_load_dwordx2 v[220:221], v[130:131], off offset:2048
	global_load_dwordx2 v[222:223], v[130:131], off offset:3584
	global_load_dwordx2 v[228:229], v[130:131], off offset:3072
	s_waitcnt vmcnt(7)
	v_and_b32_e32 v195, 0xffff0000, v132
	s_waitcnt vmcnt(6)
	v_and_b32_e32 v209, 0xffff0000, v198
	v_lshlrev_b32_e32 v194, 16, v132
	v_lshlrev_b32_e32 v208, 16, v198
	v_mul_f32_e32 v130, v195, v195
	v_mul_f32_e32 v131, v209, v209
	v_lshlrev_b32_e32 v196, 16, v133
	v_fmac_f32_e32 v130, v194, v194
	v_lshlrev_b32_e32 v210, 16, v199
	v_fmac_f32_e32 v131, v208, v208
	v_and_b32_e32 v197, 0xffff0000, v133
	v_fmac_f32_e32 v130, v196, v196
	v_and_b32_e32 v211, 0xffff0000, v199
	v_fmac_f32_e32 v131, v210, v210
	v_fmac_f32_e32 v130, v197, v197
	v_fmac_f32_e32 v131, v211, v211
	s_waitcnt vmcnt(5)
	v_and_b32_e32 v213, 0xffff0000, v200
	v_add_f32_e32 v130, v130, v131
	v_lshlrev_b32_e32 v212, 16, v200
	v_mul_f32_e32 v131, v213, v213
	v_lshlrev_b32_e32 v214, 16, v201
	v_fmac_f32_e32 v131, v212, v212
	v_and_b32_e32 v215, 0xffff0000, v201
	v_fmac_f32_e32 v131, v214, v214
	v_fmac_f32_e32 v131, v215, v215
	s_waitcnt vmcnt(4)
	v_and_b32_e32 v217, 0xffff0000, v202
	v_add_f32_e32 v130, v130, v131
	v_lshlrev_b32_e32 v216, 16, v202
	v_mul_f32_e32 v131, v217, v217
	v_lshlrev_b32_e32 v218, 16, v203
	v_fmac_f32_e32 v131, v216, v216
	v_and_b32_e32 v219, 0xffff0000, v203
	v_fmac_f32_e32 v131, v218, v218
	v_fmac_f32_e32 v131, v219, v219
	s_waitcnt vmcnt(3)
	v_and_b32_e32 v133, 0xffff0000, v204
	s_waitcnt vmcnt(2)
	v_and_b32_e32 v132, 0xffff0000, v220
	v_add_f32_e32 v193, v130, v131
	v_lshlrev_b32_e32 v131, 16, v204
	v_lshlrev_b32_e32 v130, 16, v220
	v_pk_mul_f32 v[198:199], v[132:133], v[132:133]
	v_lshlrev_b32_e32 v225, 16, v205
	v_lshlrev_b32_e32 v224, 16, v221
	v_pk_fma_f32 v[198:199], v[130:131], v[130:131], v[198:199]
	v_and_b32_e32 v227, 0xffff0000, v205
	v_and_b32_e32 v226, 0xffff0000, v221
	v_pk_fma_f32 v[198:199], v[224:225], v[224:225], v[198:199]
	s_waitcnt vmcnt(1)
	v_and_b32_e32 v201, 0xffff0000, v222
	v_pk_fma_f32 v[198:199], v[226:227], v[226:227], v[198:199]
	s_waitcnt vmcnt(0)
; DI float bflo(unsigned w) { return __uint_as_float(w << 16); }
; DI float bfhi(unsigned w) { return __uint_as_float(w & 0xffff0000u); }
; __global__ void __launch_bounds__(NWAVES * 64, 2) fwd_kernel(Args a_unused) {
;     ...
;                 for (int j = 0; j < 8; ++j) { const u32x2 w2 = *(const u32x2*)(xr + 256 * j); v[j] = (f32x4){bflo(w2[0]), bfhi(w2[0]), bflo(w2[1]), bfhi(w2[1])}; ss += v[j][0] * v[j][0] + v[j][1] * v[j][1] + v[j][2] * v[j][2] + v[j][3] * v[j][3]; }
;                 const float rstd = rsqrtf(wave_sum(ss) * (1.0f / D) + EPS);
;                 if (lane == 0) rsd[2 * wave + q] = rstd;
;                 float am = 0.f;
; #pragma unroll
;                 for (int j = 0; j < 8; ++j) { const int k = 4 * lane + 256 * j; const f32x4 g = *(const f32x4*)(A->norm_ffn_g + k), s1 = *(const f32x4*)(modl + 4 * 2048 + k), s0 = *(const f32x4*)(modl + 3 * 2048 + k);
;                     v[j] = v[j] * rstd * (g * (1.0f + s1)) + s0; am = fmaxf(am, fmaxf(fmaxf(fabsf(v[j][0]), fabsf(v[j][1])), fmaxf(fabsf(v[j][2]), fabsf(v[j][3])))); }
	v_and_b32_e32 v200, 0xffff0000, v228
	v_add_f32_e32 v193, v193, v198
	v_add_f32_e32 v193, v193, v199
	v_lshlrev_b32_e32 v199, 16, v222
	v_lshlrev_b32_e32 v198, 16, v228
	v_pk_mul_f32 v[220:221], v[200:201], v[200:201]
	v_lshlrev_b32_e32 v203, 16, v223
	v_lshlrev_b32_e32 v202, 16, v229
	v_pk_fma_f32 v[220:221], v[198:199], v[198:199], v[220:221]
	v_and_b32_e32 v205, 0xffff0000, v223
	v_and_b32_e32 v204, 0xffff0000, v229
	v_pk_fma_f32 v[220:221], v[202:203], v[202:203], v[220:221]
	s_nop 0
	v_pk_fma_f32 v[220:221], v[204:205], v[204:205], v[220:221]
	s_nop 0
	v_add_f32_e32 v193, v193, v220
	v_add_f32_e32 v193, v193, v221
	s_waitcnt lgkmcnt(0)
	s_nop 1
	v_add_f32_dpp v193, v193, v193 quad_perm:[1,0,3,2] row_mask:0xf bank_mask:0xf
	s_nop 1
	v_add_f32_dpp v193, v193, v193 quad_perm:[2,3,0,1] row_mask:0xf bank_mask:0xf
	s_nop 1
	v_add_f32_dpp v193, v193, v193 row_half_mirror row_mask:0xf bank_mask:0xf
	s_nop 1
	v_add_f32_dpp v193, v193, v193 row_mirror row_mask:0xf bank_mask:0xf
	v_mov_b32_e32 v206, v193
	s_nop 1
	v_permlane16_swap_b32 v193, v206
	v_add_f32_e32 v193, v193, v206
	v_mov_b32_e32 v206, v193
	s_nop 1
	v_permlane32_swap_b32 v193, v206
	v_add_f32_e32 v193, v193, v206
	v_fmamk_f32 v193, v193, 0x3a000000, v238
	v_mul_f32_e32 v206, 0x4b800000, v193
	v_cmp_gt_f32_e32 vcc, s39, v193
	s_nop 1
	v_cndmask_b32_e32 v193, v193, v206, vcc
	v_rsq_f32_e32 v193, v193
	s_nop 0
	v_mul_f32_e32 v206, 0x45800000, v193
	v_cndmask_b32_e32 v206, v193, v206, vcc
	s_and_saveexec_b64 s[8:9], s[4:5]
	v_mov_b32_e32 v193, s31
	ds_write_b32 v193, v206 offset:16388
	s_or_b64 exec, exec, s[8:9]
	global_load_dwordx4 v[220:223], v[144:145], off
	global_load_dwordx4 v[228:231], v[146:147], off
	global_load_dwordx4 v[242:245], v[148:149], off
	v_pk_mul_f32 v[246:247], v[206:207], v[194:195] op_sel_hi:[0,1]
	v_pk_mul_f32 v[194:195], v[206:207], v[196:197] op_sel_hi:[0,1]
	v_mov_b32_e32 v249, v226
	v_mov_b32_e32 v226, v225
	s_waitcnt vmcnt(1)
	v_pk_add_f32 v[196:197], v[230:231], 1.0 op_sel_hi:[1,0]
	v_pk_add_f32 v[228:229], v[228:229], 1.0 op_sel_hi:[1,0]
	v_pk_mul_f32 v[196:197], v[222:223], v[196:197]
	v_pk_mul_f32 v[220:221], v[220:221], v[228:229]
	s_waitcnt vmcnt(0)
	v_pk_fma_f32 v[194:195], v[196:197], v[194:195], v[244:245]
	v_pk_fma_f32 v[196:197], v[220:221], v[246:247], v[242:243]
	global_load_dwordx4 v[220:223], v[144:145], off offset:1024
	global_load_dwordx4 v[228:231], v[150:151], off
	global_load_dwordx4 v[242:245], v[152:153], off
	v_pk_mul_f32 v[246:247], v[206:207], v[208:209] op_sel_hi:[0,1]
	v_pk_mul_f32 v[208:209], v[206:207], v[210:211] op_sel_hi:[0,1]
	v_max_f32_e64 v193, |v194|, |v195|
	v_max3_f32 v193, |v196|, |v197|, v193
	s_waitcnt vmcnt(1)
	v_pk_add_f32 v[210:211], v[230:231], 1.0 op_sel_hi:[1,0]
	v_pk_add_f32 v[228:229], v[228:229], 1.0 op_sel_hi:[1,0]
	v_pk_mul_f32 v[210:211], v[222:223], v[210:211]
	v_pk_mul_f32 v[220:221], v[220:221], v[228:229]
	s_waitcnt vmcnt(0)
	v_pk_fma_f32 v[208:209], v[210:211], v[208:209], v[244:245]
	v_pk_fma_f32 v[210:211], v[220:221], v[246:247], v[242:243]
	v_max_f32_e64 v220, |v208|, |v209|
	v_max3_f32 v220, |v210|, |v211|, v220
	v_max3_f32 v193, v193, 0, v220
	global_load_dwordx4 v[220:223], v[144:145], off offset:2048
	global_load_dwordx4 v[228:231], v[154:155], off
	global_load_dwordx4 v[242:245], v[156:157], off
	v_pk_mul_f32 v[246:247], v[206:207], v[212:213] op_sel_hi:[0,1]
	v_pk_mul_f32 v[212:213], v[206:207], v[214:215] op_sel_hi:[0,1]
	s_waitcnt vmcnt(1)
	v_pk_add_f32 v[214:215], v[230:231], 1.0 op_sel_hi:[1,0]
	v_pk_add_f32 v[228:229], v[228:229], 1.0 op_sel_hi:[1,0]
	v_pk_mul_f32 v[214:215], v[222:223], v[214:215]
	v_pk_mul_f32 v[220:221], v[220:221], v[228:229]
	s_waitcnt vmcnt(0)
	v_pk_fma_f32 v[212:213], v[214:215], v[212:213], v[244:245]
	v_pk_fma_f32 v[214:215], v[220:221], v[246:247], v[242:243]
	v_max_f32_e64 v220, |v212|, |v213|
	v_max3_f32 v248, |v214|, |v215|, v220
	global_load_dwordx4 v[220:223], v[144:145], off offset:3072
	global_load_dwordx4 v[228:231], v[158:159], off
	global_load_dwordx4 v[242:245], v[160:161], off
	v_pk_mul_f32 v[246:247], v[206:207], v[216:217] op_sel_hi:[0,1]
	v_pk_mul_f32 v[216:217], v[206:207], v[218:219] op_sel_hi:[0,1]
	s_waitcnt vmcnt(1)
	v_pk_add_f32 v[218:219], v[230:231], 1.0 op_sel_hi:[1,0]
	v_pk_add_f32 v[228:229], v[228:229], 1.0 op_sel_hi:[1,0]
	v_pk_mul_f32 v[218:219], v[222:223], v[218:219]
	v_pk_mul_f32 v[220:221], v[220:221], v[228:229]
	s_waitcnt vmcnt(0)
; __global__ void __launch_bounds__(NWAVES * 64, 2) fwd_kernel(Args a_unused) {
;     ...
;                 float am = 0.f;
; #pragma unroll
;                 for (int j = 0; j < 8; ++j) { const int k = 4 * lane + 256 * j; const f32x4 g = *(const f32x4*)(A->norm_ffn_g + k), s1 = *(const f32x4*)(modl + 4 * 2048 + k), s0 = *(const f32x4*)(modl + 3 * 2048 + k);
;                     v[j] = v[j] * rstd * (g * (1.0f + s1)) + s0; am = fmaxf(am, fmaxf(fmaxf(fabsf(v[j][0]), fabsf(v[j][1])), fmaxf(fabsf(v[j][2]), fabsf(v[j][3])))); }
; #pragma unroll
;                 for (int o = 1; o < 64; o <<= 1) am = fmaxf(am, __shfl_xor(am, o));
;                 if (am == 0.f) am = 1.f;
;                 const float qi = 127.0f / am;
;                 if (lane == 0) ((float*)(ws + WS_CS + CS_ROW))[m] = am * (1.0f / 127.0f);
	v_pk_fma_f32 v[216:217], v[218:219], v[216:217], v[244:245]
	v_pk_fma_f32 v[218:219], v[220:221], v[246:247], v[242:243]
	v_max_f32_e64 v220, |v216|, |v217|
	v_max3_f32 v220, |v218|, |v219|, v220
	v_max3_f32 v193, v193, v248, v220
	global_load_dwordx4 v[220:223], v[168:169], off
	global_load_dwordx4 v[228:231], v[170:171], off
	global_load_dwordx4 v[242:245], v[172:173], off
	v_mov_b32_e32 v246, v130
	v_mov_b32_e32 v247, v132
	v_mov_b32_e32 v248, v224
	v_pk_mul_f32 v[246:247], v[206:207], v[246:247] op_sel_hi:[0,1]
	v_pk_mul_f32 v[248:249], v[206:207], v[248:249] op_sel_hi:[0,1]
	v_mov_b32_e32 v132, v131
	s_waitcnt vmcnt(1)
	v_pk_add_f32 v[230:231], v[230:231], 1.0 op_sel_hi:[1,0]
	v_pk_add_f32 v[228:229], v[228:229], 1.0 op_sel_hi:[1,0]
	v_pk_mul_f32 v[222:223], v[222:223], v[230:231]
	v_pk_mul_f32 v[228:229], v[220:221], v[228:229]
	s_waitcnt vmcnt(0)
	v_pk_fma_f32 v[220:221], v[222:223], v[248:249], v[244:245]
	v_pk_fma_f32 v[222:223], v[228:229], v[246:247], v[242:243]
	global_load_dwordx4 v[228:231], v[174:175], off
	global_load_dwordx4 v[242:245], v[176:177], off
	global_load_dwordx4 v[246:249], v[178:179], off
	v_max_f32_e64 v130, |v220|, |v221|
	v_max3_f32 v250, |v222|, |v223|, v130
	v_pk_mul_f32 v[130:131], v[206:207], v[132:133] op_sel_hi:[0,1]
	v_pk_mul_f32 v[132:133], v[206:207], v[226:227] op_sel_hi:[0,1]
	s_waitcnt vmcnt(1)
	v_pk_add_f32 v[224:225], v[244:245], 1.0 op_sel_hi:[1,0]
	v_pk_add_f32 v[226:227], v[242:243], 1.0 op_sel_hi:[1,0]
	v_pk_mul_f32 v[224:225], v[230:231], v[224:225]
	v_pk_mul_f32 v[226:227], v[228:229], v[226:227]
	s_waitcnt vmcnt(0)
	v_pk_fma_f32 v[224:225], v[224:225], v[132:133], v[248:249]
	v_pk_fma_f32 v[226:227], v[226:227], v[130:131], v[246:247]
	v_max_f32_e64 v130, |v224|, |v225|
	v_max3_f32 v130, |v226|, |v227|, v130
	v_max3_f32 v193, v193, v250, v130
	global_load_dwordx4 v[130:133], v[180:181], off
	global_load_dwordx4 v[228:231], v[182:183], off
	global_load_dwordx4 v[242:245], v[184:185], off
	v_mov_b32_e32 v248, v202
	v_mov_b32_e32 v249, v204
	v_mov_b32_e32 v246, v198
	v_mov_b32_e32 v247, v200
	v_pk_mul_f32 v[248:249], v[206:207], v[248:249] op_sel_hi:[0,1]
	v_pk_mul_f32 v[246:247], v[206:207], v[246:247] op_sel_hi:[0,1]
	v_mov_b32_e32 v200, v199
	v_mov_b32_e32 v204, v203
	v_pk_mul_f32 v[198:199], v[206:207], v[200:201] op_sel_hi:[0,1]
	v_pk_mul_f32 v[200:201], v[206:207], v[204:205] op_sel_hi:[0,1]
	s_waitcnt vmcnt(1)
	v_pk_add_f32 v[230:231], v[230:231], 1.0 op_sel_hi:[1,0]
	v_pk_add_f32 v[228:229], v[228:229], 1.0 op_sel_hi:[1,0]
	v_pk_mul_f32 v[132:133], v[132:133], v[230:231]
	v_pk_mul_f32 v[130:131], v[130:131], v[228:229]
	s_waitcnt vmcnt(0)
	v_pk_fma_f32 v[228:229], v[132:133], v[248:249], v[244:245]
	v_pk_fma_f32 v[230:231], v[130:131], v[246:247], v[242:243]
	v_max_f32_e64 v130, |v228|, |v229|
	v_max3_f32 v250, |v230|, |v231|, v130
	global_load_dwordx4 v[130:133], v[186:187], off
	global_load_dwordx4 v[242:245], v[188:189], off
	global_load_dwordx4 v[246:249], v[190:191], off
	s_waitcnt vmcnt(1)
	v_pk_add_f32 v[202:203], v[244:245], 1.0 op_sel_hi:[1,0]
	v_pk_add_f32 v[204:205], v[242:243], 1.0 op_sel_hi:[1,0]
	v_pk_mul_f32 v[132:133], v[132:133], v[202:203]
	v_pk_mul_f32 v[202:203], v[130:131], v[204:205]
	s_waitcnt vmcnt(0)
	v_pk_fma_f32 v[130:131], v[132:133], v[200:201], v[248:249]
	v_pk_fma_f32 v[132:133], v[202:203], v[198:199], v[246:247]
	v_max_f32_e64 v198, |v130|, |v131|
	v_max3_f32 v198, |v132|, |v133|, v198
	v_max3_f32 v193, v193, v250, v198
	s_waitcnt lgkmcnt(0)
	s_nop 1
	v_max_f32_dpp v193, v193, v193 quad_perm:[1,0,3,2] row_mask:0xf bank_mask:0xf
	s_nop 1
	v_max_f32_dpp v193, v193, v193 quad_perm:[2,3,0,1] row_mask:0xf bank_mask:0xf
	s_nop 1
	v_max_f32_dpp v193, v193, v193 row_half_mirror row_mask:0xf bank_mask:0xf
	s_nop 1
	v_max_f32_dpp v193, v193, v193 row_mirror row_mask:0xf bank_mask:0xf
	v_mov_b32_e32 v198, v193
	s_nop 1
	v_permlane16_swap_b32 v193, v198
	v_max_f32_e32 v193, v193, v198
	v_mov_b32_e32 v198, v193
	s_nop 1
	v_permlane32_swap_b32 v193, v198
	v_max_f32_e32 v193, v193, v198
	v_cmp_neq_f32_e32 vcc, 0, v193
	s_nop 1
	v_cndmask_b32_e32 v193, 1.0, v193, vcc
	s_and_saveexec_b64 s[8:9], s[4:5]
	s_cbranch_execz .LBB0_1871
	s_lshl_b64 s[10:11], s[6:7], 2
	s_add_u32 s10, s34, s10
	s_addc_u32 s11, s35, s11
	v_mul_f32_e32 v198, 0x3c010204, v193
	global_store_dword v165, v198, s[10:11]

; __global__ void __launch_bounds__(NWAVES * 64, 2) fwd_kernel(Args a_unused) {
;     ...
;               float f[8][4]; float am = 0.f;
; #pragma unroll
;               for (int j = 0; j < 8; ++j) { f[j][0] = __builtin_amdgcn_cvt_f32_fp8((int)v[j], 0); f[j][1] = __builtin_amdgcn_cvt_f32_fp8((int)v[j], 1); f[j][2] = __builtin_amdgcn_cvt_f32_fp8((int)v[j], 2); f[j][3] = __builtin_amdgcn_cvt_f32_fp8((int)v[j], 3);
;                   am = fmaxf(am, fmaxf(fmaxf(fabsf(f[j][0]), fabsf(f[j][1])), fmaxf(fabsf(f[j][2]), fabsf(f[j][3])))); }
; #pragma unroll
;               for (int o = 1; o < 64; o <<= 1) am = fmaxf(am, __shfl_xor(am, o));
;               if (!(am > 0.f)) am = 1.f;
;               const float qi = 127.0f / am;
;               if (lane == 0) ((float*)(ws + WS_ROUTE + RT_ARS))[m] = am * (1.0f / 127.0f);
.LBB0_2353:
	s_waitcnt vmcnt(7)
	v_cvt_f32_fp8_sdwa v27, v26 src0_sel:BYTE_3
	v_cvt_f32_fp8_sdwa v29, v26 src0_sel:BYTE_2
	v_cvt_f32_fp8_e32 v32, v26
	v_cvt_f32_fp8_sdwa v33, v26 src0_sel:BYTE_1
	v_max_f32_e64 v26, |v27|, |v27|
	v_max_f32_e64 v28, |v29|, |v29|
	v_max_f32_e32 v26, v28, v26
	v_max3_f32 v34, |v32|, |v33|, v26
	s_waitcnt vmcnt(6)
	v_cvt_f32_fp8_sdwa v26, v25 src0_sel:BYTE_3
	v_cvt_f32_fp8_sdwa v28, v25 src0_sel:BYTE_2
	v_cvt_f32_fp8_e32 v30, v25
	v_cvt_f32_fp8_sdwa v31, v25 src0_sel:BYTE_1
	v_max_f32_e64 v25, |v26|, |v26|
	v_max_f32_e64 v35, |v28|, |v28|
	v_max_f32_e32 v25, v35, v25
	v_max3_f32 v25, |v30|, |v31|, v25
	v_max3_f32 v40, v34, 0, v25
	s_waitcnt vmcnt(5)
	v_cvt_f32_fp8_sdwa v25, v24 src0_sel:BYTE_3
	v_cvt_f32_fp8_sdwa v34, v24 src0_sel:BYTE_2
	v_cvt_f32_fp8_e32 v35, v24
	v_cvt_f32_fp8_sdwa v36, v24 src0_sel:BYTE_1
	v_max_f32_e64 v24, |v25|, |v25|
	v_max_f32_e64 v37, |v34|, |v34|
	v_max_f32_e32 v24, v37, v24
	v_max3_f32 v41, |v35|, |v36|, v24
	s_waitcnt vmcnt(4)
	v_cvt_f32_fp8_sdwa v24, v23 src0_sel:BYTE_3
	v_cvt_f32_fp8_sdwa v37, v23 src0_sel:BYTE_2
	v_cvt_f32_fp8_e32 v38, v23
	v_cvt_f32_fp8_sdwa v39, v23 src0_sel:BYTE_1
	v_max_f32_e64 v23, |v24|, |v24|
	v_max_f32_e64 v42, |v37|, |v37|
	v_max_f32_e32 v23, v42, v23
	v_max3_f32 v23, |v38|, |v39|, v23
	v_max3_f32 v46, v40, v41, v23
	s_waitcnt vmcnt(3)
	v_cvt_f32_fp8_sdwa v23, v22 src0_sel:BYTE_3
	v_cvt_f32_fp8_sdwa v40, v22 src0_sel:BYTE_2
	v_cvt_f32_fp8_e32 v41, v22
	v_cvt_f32_fp8_sdwa v42, v22 src0_sel:BYTE_1
	v_max_f32_e64 v22, |v23|, |v23|
	v_max_f32_e64 v43, |v40|, |v40|
	v_max_f32_e32 v22, v43, v22
	v_max3_f32 v47, |v41|, |v42|, v22
	s_waitcnt vmcnt(2)
	v_cvt_f32_fp8_sdwa v22, v21 src0_sel:BYTE_3
	v_cvt_f32_fp8_sdwa v43, v21 src0_sel:BYTE_2
	v_cvt_f32_fp8_e32 v44, v21
	v_cvt_f32_fp8_sdwa v45, v21 src0_sel:BYTE_1
	v_max_f32_e64 v21, |v22|, |v22|
	v_max_f32_e64 v48, |v43|, |v43|
	v_max_f32_e32 v21, v48, v21
	v_max3_f32 v21, |v44|, |v45|, v21
	v_max3_f32 v51, v46, v47, v21
	s_waitcnt vmcnt(1)
	v_cvt_f32_fp8_sdwa v21, v20 src0_sel:BYTE_3
	v_cvt_f32_fp8_sdwa v46, v20 src0_sel:BYTE_2
	v_cvt_f32_fp8_e32 v47, v20
	v_cvt_f32_fp8_sdwa v48, v20 src0_sel:BYTE_1
	v_max_f32_e64 v20, |v21|, |v21|
	v_max_f32_e64 v49, |v46|, |v46|
	v_max_f32_e32 v20, v49, v20
	v_max3_f32 v52, |v47|, |v48|, v20
	s_waitcnt vmcnt(0)
	v_cvt_f32_fp8_sdwa v20, v19 src0_sel:BYTE_3
	v_cvt_f32_fp8_sdwa v49, v19 src0_sel:BYTE_2
	v_cvt_f32_fp8_e32 v50, v19
	v_cvt_f32_fp8_sdwa v19, v19 src0_sel:BYTE_1
	v_max_f32_e64 v53, |v20|, |v20|
	v_max_f32_e64 v54, |v49|, |v49|
	v_max_f32_e32 v53, v54, v53
	v_max3_f32 v53, |v50|, |v19|, v53
	v_max3_f32 v51, v51, v52, v53
	s_waitcnt lgkmcnt(0)
	s_nop 1
	v_max_f32_dpp v51, v51, v51 quad_perm:[1,0,3,2] row_mask:0xf bank_mask:0xf
	s_nop 1
	v_max_f32_dpp v51, v51, v51 quad_perm:[2,3,0,1] row_mask:0xf bank_mask:0xf
	s_nop 1
	v_max_f32_dpp v51, v51, v51 row_half_mirror row_mask:0xf bank_mask:0xf
	s_nop 1
	v_max_f32_dpp v51, v51, v51 row_mirror row_mask:0xf bank_mask:0xf
	v_mov_b32_e32 v52, v51
	s_nop 1
	v_permlane16_swap_b32 v51, v52
	v_max_f32_e32 v51, v51, v52
	v_mov_b32_e32 v52, v51
	s_nop 1
	v_permlane32_swap_b32 v51, v52
	v_max_f32_e32 v51, v51, v52
	v_cmp_lt_f32_e32 vcc, 0, v51
	s_nop 1
	v_cndmask_b32_e32 v51, 1.0, v51, vcc
	s_and_saveexec_b64 s[18:19], s[4:5]
	s_cbranch_execz .LBB0_2350
	s_add_u32 s28, s12, s20
	s_addc_u32 s29, s13, s21
	v_mul_f32_e32 v52, 0x3c010204, v51
	global_store_dword v165, v52, s[28:29]
	s_branch .LBB0_2350

; __global__ void __launch_bounds__(NWAVES * 64, 2) fwd_kernel(Args a_unused) {
;     ...
;             float ss = 0.f;
; #pragma unroll
;             for (int j = 0; j < 8; ++j) { const f32x4 m5 = *(const f32x4*)(modl + 5 * 2048 + 4 * lane + 256 * j); v[j] = v[j] + m5 * y[j]; ss += v[j][0] * v[j][0] + v[j][1] * v[j][1] + v[j][2] * v[j][2] + v[j][3] * v[j][3]; }
;             const float rstd = rsqrtf(wave_sum(ss) * (1.0f / D) + EPS);
;             float* orow = A->out + (size_t)m * D + 4 * lane;
; #pragma unroll
;             for (int j = 0; j < 8; ++j) { const f32x4 fg = *(const f32x4*)(A->final_g + 4 * lane + 256 * j); *(f32x4*)(orow + 256 * j) = v[j] * rstd * fg; }
.LBB0_2556:
	global_load_dwordx4 v[28:31], v[84:85], off
	global_load_dwordx4 v[206:209], v[84:85], off offset:1024
	global_load_dwordx4 v[210:213], v[84:85], off offset:2048
	global_load_dwordx4 v[214:217], v[84:85], off offset:3072
	global_load_dwordx4 v[218:221], v[108:109], off
	global_load_dwordx4 v[222:225], v[126:127], off
	global_load_dwordx4 v[226:229], v[128:129], off
	global_load_dwordx4 v[230:233], v[130:131], off
	global_load_dwordx4 v[234:237], v[106:107], off
	s_waitcnt vmcnt(8)
	v_pk_fma_f32 v[104:105], v[28:29], v[72:73], v[104:105]
	s_waitcnt vmcnt(7)
	v_pk_fma_f32 v[102:103], v[206:207], v[76:77], v[102:103]
	s_waitcnt vmcnt(6)
	v_pk_fma_f32 v[100:101], v[210:211], v[80:81], v[100:101]
	s_waitcnt vmcnt(5)
	v_pk_fma_f32 v[98:99], v[214:215], v[88:89], v[98:99]
	s_waitcnt vmcnt(4)
	v_pk_fma_f32 v[96:97], v[218:219], v[142:143], v[96:97]
	s_waitcnt vmcnt(3)
	v_pk_fma_f32 v[94:95], v[222:223], v[154:155], v[94:95]
	v_mul_f32_e32 v214, v105, v105
	v_mul_f32_e32 v215, v103, v103
	v_pk_fma_f32 v[124:125], v[30:31], v[70:71], v[124:125]
	v_pk_fma_f32 v[122:123], v[208:209], v[74:75], v[122:123]
	v_pk_fma_f32 v[118:119], v[216:217], v[86:87], v[118:119]
	v_mul_f32_e32 v216, v101, v101
	v_mov_b32_e32 v24, v97
	v_mov_b32_e32 v25, v95
	v_fmac_f32_e32 v214, v104, v104
	v_fmac_f32_e32 v215, v102, v102
	v_pk_fma_f32 v[120:121], v[212:213], v[78:79], v[120:121]
	v_pk_fma_f32 v[116:117], v[220:221], v[140:141], v[116:117]
	v_pk_fma_f32 v[114:115], v[224:225], v[152:153], v[114:115]
	v_mul_f32_e32 v217, v99, v99
	v_mov_b32_e32 v20, v96
	v_mov_b32_e32 v21, v94
	v_fmac_f32_e32 v216, v100, v100
	v_pk_mul_f32 v[24:25], v[24:25], v[24:25]
	v_fmac_f32_e32 v214, v124, v124
	v_fmac_f32_e32 v215, v122, v122
	s_waitcnt vmcnt(2)
	v_pk_fma_f32 v[92:93], v[226:227], v[166:167], v[92:93]
	s_waitcnt vmcnt(1)
	v_pk_fma_f32 v[90:91], v[230:231], v[170:171], v[90:91]
	v_mov_b32_e32 v28, v116
	v_mov_b32_e32 v29, v114
	v_fmac_f32_e32 v217, v98, v98
	v_fmac_f32_e32 v216, v120, v120
	v_pk_fma_f32 v[20:21], v[20:21], v[20:21], v[24:25]
	v_fmac_f32_e32 v214, v125, v125
	v_fmac_f32_e32 v215, v123, v123
	v_mov_b32_e32 v208, v93
	v_mov_b32_e32 v209, v91
	v_fmac_f32_e32 v217, v118, v118
	v_fmac_f32_e32 v216, v121, v121
	v_pk_fma_f32 v[20:21], v[28:29], v[28:29], v[20:21]
	v_add_f32_e32 v28, v214, v215
	v_pk_fma_f32 v[112:113], v[228:229], v[160:161], v[112:113]
	v_pk_fma_f32 v[110:111], v[232:233], v[168:169], v[110:111]
	v_mov_b32_e32 v30, v117
	v_mov_b32_e32 v31, v115
	v_mov_b32_e32 v206, v92
	v_mov_b32_e32 v207, v90
	v_pk_mul_f32 v[208:209], v[208:209], v[208:209]
	v_fmac_f32_e32 v217, v119, v119
	v_add_f32_e32 v28, v28, v216
	v_mov_b32_e32 v210, v112
	v_mov_b32_e32 v211, v110
	v_pk_fma_f32 v[24:25], v[206:207], v[206:207], v[208:209]
	v_pk_fma_f32 v[20:21], v[30:31], v[30:31], v[20:21]
	v_add_f32_e32 v28, v28, v217
	v_mov_b32_e32 v212, v113
	v_mov_b32_e32 v213, v111
	v_pk_fma_f32 v[24:25], v[210:211], v[210:211], v[24:25]
	v_add_f32_e32 v20, v28, v20
	v_pk_fma_f32 v[24:25], v[212:213], v[212:213], v[24:25]
	v_add_f32_e32 v20, v20, v21
	v_add_f32_e32 v20, v20, v24
	v_add_f32_e32 v20, v20, v25
	s_waitcnt lgkmcnt(0)
	s_nop 1
	v_add_f32_dpp v20, v20, v20 quad_perm:[1,0,3,2] row_mask:0xf bank_mask:0xf
	s_nop 1
	v_add_f32_dpp v20, v20, v20 quad_perm:[2,3,0,1] row_mask:0xf bank_mask:0xf
	s_nop 1
	v_add_f32_dpp v20, v20, v20 row_half_mirror row_mask:0xf bank_mask:0xf
	s_nop 1
	v_add_f32_dpp v20, v20, v20 row_mirror row_mask:0xf bank_mask:0xf
	v_mov_b32_e32 v21, v20
	s_nop 1
	v_permlane16_swap_b32 v20, v21
	v_add_f32_e32 v20, v20, v21
	v_mov_b32_e32 v21, v20
	s_nop 1
	v_permlane32_swap_b32 v20, v21
	v_add_f32_e32 v20, v20, v21
	v_fmamk_f32 v20, v20, 0x3a000000, v82
	v_mul_f32_e32 v21, 0x4b800000, v20
	v_cmp_gt_f32_e32 vcc, s18, v20
	s_nop 1
	v_cndmask_b32_e32 v20, v20, v21, vcc
	v_rsq_f32_e32 v24, v20
	v_add_co_u32_e64 v20, s[0:1], s19, v144
	v_mul_f32_e32 v25, 0x45800000, v24
	v_cndmask_b32_e32 v24, v24, v25, vcc
	v_pk_mul_f32 v[28:29], v[24:25], v[104:105] op_sel_hi:[0,1]
	v_pk_mul_f32 v[30:31], v[24:25], v[124:125] op_sel_hi:[0,1]
	v_addc_co_u32_e64 v21, s[0:1], -1, v145, s[0:1]
	s_waitcnt vmcnt(0)
	v_pk_mul_f32 v[30:31], v[236:237], v[30:31]
	v_pk_mul_f32 v[28:29], v[234:235], v[28:29]
	global_store_dwordx4 v[20:21], v[28:31], off offset:-3072
	global_load_dwordx4 v[28:31], v[106:107], off offset:1024
	v_pk_mul_f32 v[206:207], v[24:25], v[122:123] op_sel_hi:[0,1]
	v_pk_mul_f32 v[208:209], v[24:25], v[102:103] op_sel_hi:[0,1]
	s_andn2_b64 vcc, exec, s[12:13]
	s_waitcnt vmcnt(0)
	v_pk_mul_f32 v[28:29], v[28:29], v[208:209]
	v_pk_mul_f32 v[30:31], v[30:31], v[206:207]
	global_store_dwordx4 v[20:21], v[28:31], off offset:-2048
	global_load_dwordx4 v[28:31], v[106:107], off offset:2048
	v_pk_mul_f32 v[206:207], v[24:25], v[120:121] op_sel_hi:[0,1]
	v_pk_mul_f32 v[208:209], v[24:25], v[100:101] op_sel_hi:[0,1]
	s_waitcnt vmcnt(0)
	v_pk_mul_f32 v[28:29], v[28:29], v[208:209]
	v_pk_mul_f32 v[30:31], v[30:31], v[206:207]
	global_store_dwordx4 v[20:21], v[28:31], off offset:-1024
	global_load_dwordx4 v[28:31], v[106:107], off offset:3072
	v_pk_mul_f32 v[20:21], v[24:25], v[118:119] op_sel_hi:[0,1]
	v_pk_mul_f32 v[206:207], v[24:25], v[98:99] op_sel_hi:[0,1]
	s_waitcnt vmcnt(0)
	v_pk_mul_f32 v[28:29], v[28:29], v[206:207]
	v_pk_mul_f32 v[30:31], v[30:31], v[20:21]
	global_store_dwordx4 v[144:145], v[28:31], off offset:-4096
	global_load_dwordx4 v[28:31], v[132:133], off
	v_pk_mul_f32 v[20:21], v[24:25], v[116:117] op_sel_hi:[0,1]
	v_pk_mul_f32 v[206:207], v[24:25], v[96:97] op_sel_hi:[0,1]
	s_waitcnt vmcnt(0)
	v_pk_mul_f32 v[28:29], v[28:29], v[206:207]
	v_pk_mul_f32 v[30:31], v[30:31], v[20:21]
	global_store_dwordx4 v[144:145], v[28:31], off offset:-3072
	global_load_dwordx4 v[28:31], v[134:135], off
	v_pk_mul_f32 v[20:21], v[24:25], v[114:115] op_sel_hi:[0,1]
	v_pk_mul_f32 v[206:207], v[24:25], v[94:95] op_sel_hi:[0,1]
	s_waitcnt vmcnt(0)
	v_pk_mul_f32 v[28:29], v[28:29], v[206:207]
	v_pk_mul_f32 v[30:31], v[30:31], v[20:21]
	global_store_dwordx4 v[144:145], v[28:31], off offset:-2048
	global_load_dwordx4 v[28:31], v[136:137], off
	v_pk_mul_f32 v[20:21], v[24:25], v[112:113] op_sel_hi:[0,1]
	v_pk_mul_f32 v[206:207], v[24:25], v[92:93] op_sel_hi:[0,1]
	s_waitcnt vmcnt(0)
	v_pk_mul_f32 v[28:29], v[28:29], v[206:207]
	v_pk_mul_f32 v[30:31], v[30:31], v[20:21]
	global_store_dwordx4 v[144:145], v[28:31], off offset:-1024
	global_load_dwordx4 v[28:31], v[138:139], off
	v_pk_mul_f32 v[20:21], v[24:25], v[110:111] op_sel_hi:[0,1]
	v_pk_mul_f32 v[24:25], v[24:25], v[90:91] op_sel_hi:[0,1]
	s_waitcnt vmcnt(0)
	v_pk_mul_f32 v[28:29], v[28:29], v[24:25]
	v_pk_mul_f32 v[30:31], v[30:31], v[20:21]
	global_store_dwordx4 v[144:145], v[28:31], off
	s_cbranch_vccnz .LBB0_2551
	v_cvt_f32_i32_sdwa v25, sext(v39) dst_sel:DWORD dst_unused:UNUSED_PAD src0_sel:BYTE_2
	v_cvt_f32_i32_sdwa v21, sext(v39) dst_sel:DWORD dst_unused:UNUSED_PAD src0_sel:BYTE_3
	v_cvt_f32_i32_sdwa v20, sext(v38) dst_sel:DWORD dst_unused:UNUSED_PAD src0_sel:BYTE_3
	v_cvt_f32_i32_sdwa v24, sext(v38) dst_sel:DWORD dst_unused:UNUSED_PAD src0_sel:BYTE_2
	v_mul_f32_e32 v28, v5, v25
	v_cvt_f32_i32_sdwa v25, sext(v55) dst_sel:DWORD dst_unused:UNUSED_PAD src0_sel:BYTE_2
	v_cvt_f32_i32_sdwa v29, sext(v54) dst_sel:DWORD dst_unused:UNUSED_PAD src0_sel:BYTE_2
	v_cvt_f32_i32_sdwa v71, sext(v38) dst_sel:DWORD dst_unused:UNUSED_PAD src0_sel:BYTE_1
	v_cvt_f32_i32_sdwa v70, sext(v38) dst_sel:DWORD dst_unused:UNUSED_PAD src0_sel:BYTE_0
	v_cvt_f32_i32_sdwa v73, sext(v39) dst_sel:DWORD dst_unused:UNUSED_PAD src0_sel:BYTE_1
	v_cvt_f32_i32_sdwa v72, sext(v39) dst_sel:DWORD dst_unused:UNUSED_PAD src0_sel:BYTE_0
	v_pk_mul_f32 v[20:21], v[4:5], v[20:21]
	v_cvt_f32_i32_sdwa v75, sext(v54) dst_sel:DWORD dst_unused:UNUSED_PAD src0_sel:BYTE_1
	v_cvt_f32_i32_sdwa v74, sext(v54) dst_sel:DWORD dst_unused:UNUSED_PAD src0_sel:BYTE_0
	v_mul_f32_e32 v24, v4, v24
	v_cvt_f32_i32_sdwa v77, sext(v55) dst_sel:DWORD dst_unused:UNUSED_PAD src0_sel:BYTE_3
	v_cvt_f32_i32_sdwa v76, sext(v54) dst_sel:DWORD dst_unused:UNUSED_PAD src0_sel:BYTE_3
	v_cvt_f32_i32_sdwa v79, sext(v55) dst_sel:DWORD dst_unused:UNUSED_PAD src0_sel:BYTE_1
	v_cvt_f32_i32_sdwa v78, sext(v55) dst_sel:DWORD dst_unused:UNUSED_PAD src0_sel:BYTE_0
	v_mul_f32_e32 v80, v17, v25
	v_mov_b32_e32 v25, v20
	v_mul_f32_e32 v30, v16, v29
	v_mov_b32_e32 v29, v21
	v_pk_add_f32 v[20:21], v[24:25], 0 op_sel_hi:[1,0]
	v_pk_fma_f32 v[24:25], v[4:5], v[70:71], 0 op_sel_hi:[0,1,0]
	v_pk_fma_f32 v[24:25], v[4:5], v[72:73], v[24:25] op_sel:[1,0,0]
	v_pk_mul_f32 v[76:77], v[16:17], v[76:77]
	v_pk_fma_f32 v[24:25], v[16:17], v[74:75], v[24:25] op_sel_hi:[0,1,1]
	v_pk_fma_f32 v[72:73], v[16:17], v[78:79], v[24:25] op_sel:[1,0,0]
	v_cvt_f32_i32_sdwa v25, sext(v41) dst_sel:DWORD dst_unused:UNUSED_PAD src0_sel:BYTE_2
	v_mov_b32_e32 v31, v76
	v_pk_add_f32 v[20:21], v[20:21], v[28:29]
	v_mov_b32_e32 v81, v77
	v_pk_add_f32 v[20:21], v[20:21], v[30:31]
	v_cvt_f32_i32_sdwa v24, sext(v40) dst_sel:DWORD dst_unused:UNUSED_PAD src0_sel:BYTE_2
	v_pk_add_f32 v[70:71], v[20:21], v[80:81]
	v_cvt_f32_i32_sdwa v21, sext(v41) dst_sel:DWORD dst_unused:UNUSED_PAD src0_sel:BYTE_3
	v_cvt_f32_i32_sdwa v20, sext(v40) dst_sel:DWORD dst_unused:UNUSED_PAD src0_sel:BYTE_3
	v_mul_f32_e32 v28, v27, v25
	v_cvt_f32_i32_sdwa v25, sext(v57) dst_sel:DWORD dst_unused:UNUSED_PAD src0_sel:BYTE_2
	v_cvt_f32_i32_sdwa v29, sext(v56) dst_sel:DWORD dst_unused:UNUSED_PAD src0_sel:BYTE_2
	v_cvt_f32_i32_sdwa v75, sext(v40) dst_sel:DWORD dst_unused:UNUSED_PAD src0_sel:BYTE_1
	v_cvt_f32_i32_sdwa v74, sext(v40) dst_sel:DWORD dst_unused:UNUSED_PAD src0_sel:BYTE_0
	v_cvt_f32_i32_sdwa v77, sext(v41) dst_sel:DWORD dst_unused:UNUSED_PAD src0_sel:BYTE_1
	v_cvt_f32_i32_sdwa v76, sext(v41) dst_sel:DWORD dst_unused:UNUSED_PAD src0_sel:BYTE_0
	v_pk_mul_f32 v[20:21], v[26:27], v[20:21]
	v_cvt_f32_i32_sdwa v79, sext(v56) dst_sel:DWORD dst_unused:UNUSED_PAD src0_sel:BYTE_1
	v_cvt_f32_i32_sdwa v78, sext(v56) dst_sel:DWORD dst_unused:UNUSED_PAD src0_sel:BYTE_0
	v_mul_f32_e32 v24, v26, v24
	v_cvt_f32_i32_sdwa v81, sext(v57) dst_sel:DWORD dst_unused:UNUSED_PAD src0_sel:BYTE_3
	v_cvt_f32_i32_sdwa v80, sext(v56) dst_sel:DWORD dst_unused:UNUSED_PAD src0_sel:BYTE_3
	v_cvt_f32_i32_sdwa v87, sext(v57) dst_sel:DWORD dst_unused:UNUSED_PAD src0_sel:BYTE_1
	v_cvt_f32_i32_sdwa v86, sext(v57) dst_sel:DWORD dst_unused:UNUSED_PAD src0_sel:BYTE_0
	v_mul_f32_e32 v88, v23, v25
	v_mov_b32_e32 v25, v20
	v_mul_f32_e32 v30, v22, v29
	v_mov_b32_e32 v29, v21
	v_pk_add_f32 v[20:21], v[24:25], 0 op_sel_hi:[1,0]
	v_pk_fma_f32 v[24:25], v[26:27], v[74:75], 0 op_sel_hi:[0,1,0]
	v_pk_fma_f32 v[24:25], v[26:27], v[76:77], v[24:25] op_sel:[1,0,0]
	v_pk_mul_f32 v[80:81], v[22:23], v[80:81]
	v_pk_fma_f32 v[24:25], v[22:23], v[78:79], v[24:25] op_sel_hi:[0,1,1]
	v_pk_fma_f32 v[76:77], v[22:23], v[86:87], v[24:25] op_sel:[1,0,0]
	v_cvt_f32_i32_sdwa v25, sext(v43) dst_sel:DWORD dst_unused:UNUSED_PAD src0_sel:BYTE_2
	v_mov_b32_e32 v31, v80
	v_pk_add_f32 v[20:21], v[20:21], v[28:29]
	v_mov_b32_e32 v89, v81
	v_pk_add_f32 v[20:21], v[20:21], v[30:31]
	v_cvt_f32_i32_sdwa v24, sext(v42) dst_sel:DWORD dst_unused:UNUSED_PAD src0_sel:BYTE_2
	v_pk_add_f32 v[74:75], v[20:21], v[88:89]
	v_cvt_f32_i32_sdwa v21, sext(v43) dst_sel:DWORD dst_unused:UNUSED_PAD src0_sel:BYTE_3
	v_cvt_f32_i32_sdwa v20, sext(v42) dst_sel:DWORD dst_unused:UNUSED_PAD src0_sel:BYTE_3
	v_mul_f32_e32 v28, v7, v25
	v_cvt_f32_i32_sdwa v25, sext(v59) dst_sel:DWORD dst_unused:UNUSED_PAD src0_sel:BYTE_2
	v_cvt_f32_i32_sdwa v29, sext(v58) dst_sel:DWORD dst_unused:UNUSED_PAD src0_sel:BYTE_2
	v_cvt_f32_i32_sdwa v79, sext(v42) dst_sel:DWORD dst_unused:UNUSED_PAD src0_sel:BYTE_1
	v_cvt_f32_i32_sdwa v78, sext(v42) dst_sel:DWORD dst_unused:UNUSED_PAD src0_sel:BYTE_0
	v_cvt_f32_i32_sdwa v81, sext(v43) dst_sel:DWORD dst_unused:UNUSED_PAD src0_sel:BYTE_1
	v_cvt_f32_i32_sdwa v80, sext(v43) dst_sel:DWORD dst_unused:UNUSED_PAD src0_sel:BYTE_0
	v_pk_mul_f32 v[20:21], v[6:7], v[20:21]
	v_cvt_f32_i32_sdwa v87, sext(v58) dst_sel:DWORD dst_unused:UNUSED_PAD src0_sel:BYTE_1
	v_cvt_f32_i32_sdwa v86, sext(v58) dst_sel:DWORD dst_unused:UNUSED_PAD src0_sel:BYTE_0
	v_mul_f32_e32 v24, v6, v24
	v_cvt_f32_i32_sdwa v89, sext(v59) dst_sel:DWORD dst_unused:UNUSED_PAD src0_sel:BYTE_3
	v_cvt_f32_i32_sdwa v88, sext(v58) dst_sel:DWORD dst_unused:UNUSED_PAD src0_sel:BYTE_3
	v_cvt_f32_i32_sdwa v91, sext(v59) dst_sel:DWORD dst_unused:UNUSED_PAD src0_sel:BYTE_1
	v_cvt_f32_i32_sdwa v90, sext(v59) dst_sel:DWORD dst_unused:UNUSED_PAD src0_sel:BYTE_0
	v_mul_f32_e32 v92, v19, v25
	v_mov_b32_e32 v25, v20
	v_mul_f32_e32 v30, v18, v29
	v_mov_b32_e32 v29, v21
	v_pk_add_f32 v[20:21], v[24:25], 0 op_sel_hi:[1,0]
	v_pk_fma_f32 v[24:25], v[6:7], v[78:79], 0 op_sel_hi:[0,1,0]
	v_pk_fma_f32 v[24:25], v[6:7], v[80:81], v[24:25] op_sel:[1,0,0]
	v_pk_mul_f32 v[88:89], v[18:19], v[88:89]
	v_pk_fma_f32 v[24:25], v[18:19], v[86:87], v[24:25] op_sel_hi:[0,1,1]
	v_pk_fma_f32 v[80:81], v[18:19], v[90:91], v[24:25] op_sel:[1,0,0]
	v_cvt_f32_i32_sdwa v25, sext(v45) dst_sel:DWORD dst_unused:UNUSED_PAD src0_sel:BYTE_2
	v_mov_b32_e32 v31, v88
	v_pk_add_f32 v[20:21], v[20:21], v[28:29]
	v_mov_b32_e32 v93, v89
	v_pk_add_f32 v[20:21], v[20:21], v[30:31]
	v_cvt_f32_i32_sdwa v24, sext(v44) dst_sel:DWORD dst_unused:UNUSED_PAD src0_sel:BYTE_2
	v_pk_add_f32 v[78:79], v[20:21], v[92:93]
	v_cvt_f32_i32_sdwa v21, sext(v45) dst_sel:DWORD dst_unused:UNUSED_PAD src0_sel:BYTE_3
	v_cvt_f32_i32_sdwa v20, sext(v44) dst_sel:DWORD dst_unused:UNUSED_PAD src0_sel:BYTE_3
	v_mul_f32_e32 v28, v159, v25
	v_cvt_f32_i32_sdwa v25, sext(v61) dst_sel:DWORD dst_unused:UNUSED_PAD src0_sel:BYTE_2
	v_cvt_f32_i32_sdwa v29, sext(v60) dst_sel:DWORD dst_unused:UNUSED_PAD src0_sel:BYTE_2
	v_cvt_f32_i32_sdwa v87, sext(v44) dst_sel:DWORD dst_unused:UNUSED_PAD src0_sel:BYTE_1
	v_cvt_f32_i32_sdwa v86, sext(v44) dst_sel:DWORD dst_unused:UNUSED_PAD src0_sel:BYTE_0
	v_cvt_f32_i32_sdwa v89, sext(v45) dst_sel:DWORD dst_unused:UNUSED_PAD src0_sel:BYTE_1
	v_cvt_f32_i32_sdwa v88, sext(v45) dst_sel:DWORD dst_unused:UNUSED_PAD src0_sel:BYTE_0
	v_pk_mul_f32 v[20:21], v[158:159], v[20:21]
	v_cvt_f32_i32_sdwa v91, sext(v60) dst_sel:DWORD dst_unused:UNUSED_PAD src0_sel:BYTE_1
	v_cvt_f32_i32_sdwa v90, sext(v60) dst_sel:DWORD dst_unused:UNUSED_PAD src0_sel:BYTE_0
	v_mul_f32_e32 v24, v158, v24
	v_cvt_f32_i32_sdwa v93, sext(v61) dst_sel:DWORD dst_unused:UNUSED_PAD src0_sel:BYTE_3
	v_cvt_f32_i32_sdwa v92, sext(v60) dst_sel:DWORD dst_unused:UNUSED_PAD src0_sel:BYTE_3
	v_cvt_f32_i32_sdwa v95, sext(v61) dst_sel:DWORD dst_unused:UNUSED_PAD src0_sel:BYTE_1
	v_cvt_f32_i32_sdwa v94, sext(v61) dst_sel:DWORD dst_unused:UNUSED_PAD src0_sel:BYTE_0
	v_mul_f32_e32 v96, v33, v25
	v_mov_b32_e32 v25, v20
	v_mul_f32_e32 v30, v32, v29
	v_mov_b32_e32 v29, v21
	v_pk_add_f32 v[20:21], v[24:25], 0 op_sel_hi:[1,0]
	v_pk_fma_f32 v[24:25], v[158:159], v[86:87], 0 op_sel_hi:[0,1,0]
	v_pk_fma_f32 v[24:25], v[158:159], v[88:89], v[24:25] op_sel:[1,0,0]
	v_pk_mul_f32 v[92:93], v[32:33], v[92:93]
	v_pk_fma_f32 v[24:25], v[32:33], v[90:91], v[24:25] op_sel_hi:[0,1,1]
	v_pk_fma_f32 v[88:89], v[32:33], v[94:95], v[24:25] op_sel:[1,0,0]
	v_cvt_f32_i32_sdwa v25, sext(v47) dst_sel:DWORD dst_unused:UNUSED_PAD src0_sel:BYTE_2
	v_mov_b32_e32 v31, v92
	v_pk_add_f32 v[20:21], v[20:21], v[28:29]
	v_mov_b32_e32 v97, v93
	v_pk_add_f32 v[20:21], v[20:21], v[30:31]
	v_cvt_f32_i32_sdwa v24, sext(v46) dst_sel:DWORD dst_unused:UNUSED_PAD src0_sel:BYTE_2
	v_pk_add_f32 v[86:87], v[20:21], v[96:97]
	v_cvt_f32_i32_sdwa v21, sext(v47) dst_sel:DWORD dst_unused:UNUSED_PAD src0_sel:BYTE_3
	v_cvt_f32_i32_sdwa v20, sext(v46) dst_sel:DWORD dst_unused:UNUSED_PAD src0_sel:BYTE_3
	v_mul_f32_e32 v28, v1, v25
	v_cvt_f32_i32_sdwa v25, sext(v63) dst_sel:DWORD dst_unused:UNUSED_PAD src0_sel:BYTE_2
	v_cvt_f32_i32_sdwa v29, sext(v62) dst_sel:DWORD dst_unused:UNUSED_PAD src0_sel:BYTE_2
	v_cvt_f32_i32_sdwa v91, sext(v46) dst_sel:DWORD dst_unused:UNUSED_PAD src0_sel:BYTE_1
	v_cvt_f32_i32_sdwa v90, sext(v46) dst_sel:DWORD dst_unused:UNUSED_PAD src0_sel:BYTE_0
	v_cvt_f32_i32_sdwa v93, sext(v47) dst_sel:DWORD dst_unused:UNUSED_PAD src0_sel:BYTE_1
	v_cvt_f32_i32_sdwa v92, sext(v47) dst_sel:DWORD dst_unused:UNUSED_PAD src0_sel:BYTE_0
	v_pk_mul_f32 v[20:21], v[0:1], v[20:21]
	v_cvt_f32_i32_sdwa v95, sext(v62) dst_sel:DWORD dst_unused:UNUSED_PAD src0_sel:BYTE_1
	v_cvt_f32_i32_sdwa v94, sext(v62) dst_sel:DWORD dst_unused:UNUSED_PAD src0_sel:BYTE_0
	v_mul_f32_e32 v24, v0, v24
	v_cvt_f32_i32_sdwa v97, sext(v63) dst_sel:DWORD dst_unused:UNUSED_PAD src0_sel:BYTE_3
	v_cvt_f32_i32_sdwa v96, sext(v62) dst_sel:DWORD dst_unused:UNUSED_PAD src0_sel:BYTE_3
	v_cvt_f32_i32_sdwa v99, sext(v63) dst_sel:DWORD dst_unused:UNUSED_PAD src0_sel:BYTE_1
	v_cvt_f32_i32_sdwa v98, sext(v63) dst_sel:DWORD dst_unused:UNUSED_PAD src0_sel:BYTE_0
	v_mul_f32_e32 v100, v13, v25
	v_mov_b32_e32 v25, v20
	v_mul_f32_e32 v30, v12, v29
	v_mov_b32_e32 v29, v21
	v_pk_add_f32 v[20:21], v[24:25], 0 op_sel_hi:[1,0]
	v_pk_fma_f32 v[24:25], v[0:1], v[90:91], 0 op_sel_hi:[0,1,0]
	v_pk_fma_f32 v[24:25], v[0:1], v[92:93], v[24:25] op_sel:[1,0,0]
	v_pk_mul_f32 v[96:97], v[12:13], v[96:97]
	v_pk_fma_f32 v[24:25], v[12:13], v[94:95], v[24:25] op_sel_hi:[0,1,1]
	v_pk_fma_f32 v[142:143], v[12:13], v[98:99], v[24:25] op_sel:[1,0,0]
	v_cvt_f32_i32_sdwa v25, sext(v49) dst_sel:DWORD dst_unused:UNUSED_PAD src0_sel:BYTE_2
	v_mov_b32_e32 v31, v96
	v_pk_add_f32 v[20:21], v[20:21], v[28:29]
	v_mov_b32_e32 v101, v97
	v_pk_add_f32 v[20:21], v[20:21], v[30:31]
	v_cvt_f32_i32_sdwa v24, sext(v48) dst_sel:DWORD dst_unused:UNUSED_PAD src0_sel:BYTE_2
	v_pk_add_f32 v[140:141], v[20:21], v[100:101]
	v_cvt_f32_i32_sdwa v21, sext(v49) dst_sel:DWORD dst_unused:UNUSED_PAD src0_sel:BYTE_3
	v_cvt_f32_i32_sdwa v20, sext(v48) dst_sel:DWORD dst_unused:UNUSED_PAD src0_sel:BYTE_3
	v_mul_f32_e32 v28, v157, v25
	v_cvt_f32_i32_sdwa v25, sext(v65) dst_sel:DWORD dst_unused:UNUSED_PAD src0_sel:BYTE_2
	v_cvt_f32_i32_sdwa v29, sext(v64) dst_sel:DWORD dst_unused:UNUSED_PAD src0_sel:BYTE_2
	v_cvt_f32_i32_sdwa v91, sext(v48) dst_sel:DWORD dst_unused:UNUSED_PAD src0_sel:BYTE_1
; __global__ void __launch_bounds__(NWAVES * 64, 2) fwd_kernel(Args a_unused) {
;     ...
;             if (more) { P12_SUM();
; #pragma unroll
;                 for (int j = 0; j < 8; ++j) v[j] = vn[j]; }
	v_cvt_f32_i32_sdwa v90, sext(v48) dst_sel:DWORD dst_unused:UNUSED_PAD src0_sel:BYTE_0
	v_cvt_f32_i32_sdwa v93, sext(v49) dst_sel:DWORD dst_unused:UNUSED_PAD src0_sel:BYTE_1
	v_cvt_f32_i32_sdwa v92, sext(v49) dst_sel:DWORD dst_unused:UNUSED_PAD src0_sel:BYTE_0
	v_pk_mul_f32 v[20:21], v[156:157], v[20:21]
	v_cvt_f32_i32_sdwa v95, sext(v64) dst_sel:DWORD dst_unused:UNUSED_PAD src0_sel:BYTE_1
	v_cvt_f32_i32_sdwa v94, sext(v64) dst_sel:DWORD dst_unused:UNUSED_PAD src0_sel:BYTE_0
	v_mul_f32_e32 v24, v156, v24
	v_cvt_f32_i32_sdwa v97, sext(v65) dst_sel:DWORD dst_unused:UNUSED_PAD src0_sel:BYTE_3
	v_cvt_f32_i32_sdwa v96, sext(v64) dst_sel:DWORD dst_unused:UNUSED_PAD src0_sel:BYTE_3
	v_cvt_f32_i32_sdwa v99, sext(v65) dst_sel:DWORD dst_unused:UNUSED_PAD src0_sel:BYTE_1
	v_cvt_f32_i32_sdwa v98, sext(v65) dst_sel:DWORD dst_unused:UNUSED_PAD src0_sel:BYTE_0
	v_mul_f32_e32 v100, v35, v25
	v_mov_b32_e32 v25, v20
	v_mul_f32_e32 v30, v34, v29
	v_mov_b32_e32 v29, v21
	v_pk_add_f32 v[20:21], v[24:25], 0 op_sel_hi:[1,0]
	v_pk_fma_f32 v[24:25], v[156:157], v[90:91], 0 op_sel_hi:[0,1,0]
	v_pk_fma_f32 v[24:25], v[156:157], v[92:93], v[24:25] op_sel:[1,0,0]
	v_pk_mul_f32 v[96:97], v[34:35], v[96:97]
	v_pk_fma_f32 v[24:25], v[34:35], v[94:95], v[24:25] op_sel_hi:[0,1,1]
	v_pk_fma_f32 v[154:155], v[34:35], v[98:99], v[24:25] op_sel:[1,0,0]
	v_cvt_f32_i32_sdwa v25, sext(v51) dst_sel:DWORD dst_unused:UNUSED_PAD src0_sel:BYTE_2
	v_mov_b32_e32 v31, v96
	v_pk_add_f32 v[20:21], v[20:21], v[28:29]
	v_mov_b32_e32 v101, v97
	v_pk_add_f32 v[20:21], v[20:21], v[30:31]
	v_cvt_f32_i32_sdwa v24, sext(v50) dst_sel:DWORD dst_unused:UNUSED_PAD src0_sel:BYTE_2
	v_pk_add_f32 v[152:153], v[20:21], v[100:101]
	v_cvt_f32_i32_sdwa v21, sext(v51) dst_sel:DWORD dst_unused:UNUSED_PAD src0_sel:BYTE_3
	v_cvt_f32_i32_sdwa v20, sext(v50) dst_sel:DWORD dst_unused:UNUSED_PAD src0_sel:BYTE_3
	v_mul_f32_e32 v28, v3, v25
	v_cvt_f32_i32_sdwa v25, sext(v67) dst_sel:DWORD dst_unused:UNUSED_PAD src0_sel:BYTE_2
	v_cvt_f32_i32_sdwa v29, sext(v66) dst_sel:DWORD dst_unused:UNUSED_PAD src0_sel:BYTE_2
	v_cvt_f32_i32_sdwa v91, sext(v50) dst_sel:DWORD dst_unused:UNUSED_PAD src0_sel:BYTE_1
	v_cvt_f32_i32_sdwa v90, sext(v50) dst_sel:DWORD dst_unused:UNUSED_PAD src0_sel:BYTE_0
	v_cvt_f32_i32_sdwa v93, sext(v51) dst_sel:DWORD dst_unused:UNUSED_PAD src0_sel:BYTE_1
	v_cvt_f32_i32_sdwa v92, sext(v51) dst_sel:DWORD dst_unused:UNUSED_PAD src0_sel:BYTE_0
	v_pk_mul_f32 v[20:21], v[2:3], v[20:21]
	v_cvt_f32_i32_sdwa v95, sext(v66) dst_sel:DWORD dst_unused:UNUSED_PAD src0_sel:BYTE_1
	v_cvt_f32_i32_sdwa v94, sext(v66) dst_sel:DWORD dst_unused:UNUSED_PAD src0_sel:BYTE_0
	v_mul_f32_e32 v24, v2, v24
	v_cvt_f32_i32_sdwa v97, sext(v67) dst_sel:DWORD dst_unused:UNUSED_PAD src0_sel:BYTE_3
	v_cvt_f32_i32_sdwa v96, sext(v66) dst_sel:DWORD dst_unused:UNUSED_PAD src0_sel:BYTE_3
	v_cvt_f32_i32_sdwa v99, sext(v67) dst_sel:DWORD dst_unused:UNUSED_PAD src0_sel:BYTE_1
	v_cvt_f32_i32_sdwa v98, sext(v67) dst_sel:DWORD dst_unused:UNUSED_PAD src0_sel:BYTE_0
	v_mul_f32_e32 v100, v15, v25
	v_mov_b32_e32 v25, v20
	v_mul_f32_e32 v30, v14, v29
	v_mov_b32_e32 v29, v21
	v_pk_add_f32 v[20:21], v[24:25], 0 op_sel_hi:[1,0]
	v_pk_fma_f32 v[24:25], v[2:3], v[90:91], 0 op_sel_hi:[0,1,0]
	v_pk_fma_f32 v[24:25], v[2:3], v[92:93], v[24:25] op_sel:[1,0,0]
	v_pk_mul_f32 v[96:97], v[14:15], v[96:97]
	v_pk_fma_f32 v[24:25], v[14:15], v[94:95], v[24:25] op_sel_hi:[0,1,1]
	v_pk_fma_f32 v[166:167], v[14:15], v[98:99], v[24:25] op_sel:[1,0,0]
	v_cvt_f32_i32_sdwa v25, sext(v53) dst_sel:DWORD dst_unused:UNUSED_PAD src0_sel:BYTE_2
	v_mov_b32_e32 v31, v96
	v_pk_add_f32 v[20:21], v[20:21], v[28:29]
	v_mov_b32_e32 v101, v97
	v_pk_add_f32 v[20:21], v[20:21], v[30:31]
	v_cvt_f32_i32_sdwa v24, sext(v52) dst_sel:DWORD dst_unused:UNUSED_PAD src0_sel:BYTE_2
	v_pk_add_f32 v[160:161], v[20:21], v[100:101]
	v_cvt_f32_i32_sdwa v21, sext(v53) dst_sel:DWORD dst_unused:UNUSED_PAD src0_sel:BYTE_3
	v_cvt_f32_i32_sdwa v20, sext(v52) dst_sel:DWORD dst_unused:UNUSED_PAD src0_sel:BYTE_3
	v_mul_f32_e32 v28, v151, v25
	v_cvt_f32_i32_sdwa v25, sext(v69) dst_sel:DWORD dst_unused:UNUSED_PAD src0_sel:BYTE_2
	v_cvt_f32_i32_sdwa v29, sext(v68) dst_sel:DWORD dst_unused:UNUSED_PAD src0_sel:BYTE_2
	v_cvt_f32_i32_sdwa v91, sext(v52) dst_sel:DWORD dst_unused:UNUSED_PAD src0_sel:BYTE_1
	v_cvt_f32_i32_sdwa v90, sext(v52) dst_sel:DWORD dst_unused:UNUSED_PAD src0_sel:BYTE_0
	v_cvt_f32_i32_sdwa v97, sext(v69) dst_sel:DWORD dst_unused:UNUSED_PAD src0_sel:BYTE_3
	v_cvt_f32_i32_sdwa v96, sext(v68) dst_sel:DWORD dst_unused:UNUSED_PAD src0_sel:BYTE_3
	v_cvt_f32_i32_sdwa v93, sext(v53) dst_sel:DWORD dst_unused:UNUSED_PAD src0_sel:BYTE_1
	v_cvt_f32_i32_sdwa v92, sext(v53) dst_sel:DWORD dst_unused:UNUSED_PAD src0_sel:BYTE_0
	v_pk_mul_f32 v[20:21], v[150:151], v[20:21]
	v_cvt_f32_i32_sdwa v95, sext(v68) dst_sel:DWORD dst_unused:UNUSED_PAD src0_sel:BYTE_1
	v_cvt_f32_i32_sdwa v94, sext(v68) dst_sel:DWORD dst_unused:UNUSED_PAD src0_sel:BYTE_0
	v_mul_f32_e32 v24, v150, v24
	v_cvt_f32_i32_sdwa v99, sext(v69) dst_sel:DWORD dst_unused:UNUSED_PAD src0_sel:BYTE_1
	v_cvt_f32_i32_sdwa v98, sext(v69) dst_sel:DWORD dst_unused:UNUSED_PAD src0_sel:BYTE_0
	v_mul_f32_e32 v100, v149, v25
	v_mov_b32_e32 v25, v20
	v_mul_f32_e32 v30, v148, v29
	v_pk_mul_f32 v[96:97], v[148:149], v[96:97]
	v_mov_b32_e32 v29, v21
	v_pk_add_f32 v[20:21], v[24:25], 0 op_sel_hi:[1,0]
	v_pk_fma_f32 v[24:25], v[150:151], v[90:91], 0 op_sel_hi:[0,1,0]
	v_mov_b32_e32 v31, v96
	v_pk_add_f32 v[20:21], v[20:21], v[28:29]
	v_pk_fma_f32 v[24:25], v[150:151], v[92:93], v[24:25] op_sel:[1,0,0]
	v_mov_b32_e32 v101, v97
	v_pk_add_f32 v[20:21], v[20:21], v[30:31]
	v_pk_fma_f32 v[24:25], v[148:149], v[94:95], v[24:25] op_sel_hi:[0,1,1]
	v_pk_add_f32 v[168:169], v[20:21], v[100:101]
	v_pk_fma_f32 v[170:171], v[148:149], v[98:99], v[24:25] op_sel:[1,0,0]
	v_mov_b32_e32 v90, v162
	v_mov_b32_e32 v91, v175
	v_mov_b32_e32 v110, v190
	v_mov_b32_e32 v111, v198
	v_mov_b32_e32 v92, v163
	v_mov_b32_e32 v93, v183
	v_mov_b32_e32 v112, v191
	v_mov_b32_e32 v113, v199
	v_mov_b32_e32 v94, v164
	v_mov_b32_e32 v95, v184
	v_mov_b32_e32 v114, v192
	v_mov_b32_e32 v115, v200
	v_mov_b32_e32 v96, v165
	v_mov_b32_e32 v97, v185
	v_mov_b32_e32 v116, v193
	v_mov_b32_e32 v117, v201
	v_mov_b32_e32 v98, v172
	v_mov_b32_e32 v99, v186
	v_mov_b32_e32 v118, v194
	v_mov_b32_e32 v119, v202
	v_mov_b32_e32 v100, v173
	v_mov_b32_e32 v101, v187
	v_mov_b32_e32 v120, v195
	v_mov_b32_e32 v121, v203
	v_mov_b32_e32 v102, v174
	v_mov_b32_e32 v103, v188
	v_mov_b32_e32 v122, v196
	v_mov_b32_e32 v123, v204
	v_mov_b32_e32 v104, v182
	v_mov_b32_e32 v105, v189
	v_mov_b32_e32 v124, v197
	v_mov_b32_e32 v125, v205
	s_branch .LBB0_2551
